# stagger: half of the workgroups (blockIdx bit 3) s_sleep 40..127 at the start of each GEMM phase to de-synchronize epilogue store bursts
# speedup vs baseline: 1.0084x; 1.0084x over previous
; #define PG8_STAGE(bufoff, gbase, voff) do { _Pragma("unroll") for (int _i = 0; _i < 2; ++_i) \
;         __builtin_amdgcn_global_load_lds((const unsigned*)((const char*)(gbase) + (voff)[_i]), (PG8_LAS unsigned*)(lds + (bufoff) + ldsw + _i * 8192), 16, 0, 0); } while (0)
; #define PG8_BAR __builtin_amdgcn_s_barrier()
; template <class Epi, class Sched, bool ALIGN_EPI = false, bool SP2 = false, bool FP8 = false, bool ABLK = false>
; __device__ __forceinline__ void gemm_phase(PG8_LAS unsigned char* lds, const Gemm g, const Sched& S, const Epi& E) {
;     int tid_ = threadIdx.x; asm volatile("" : "+v"(tid_));
;     const int tid = tid_, wid = __builtin_amdgcn_readfirstlane(tid >> 6), lane = tid & 63, wr = wid >> 2, wc = wid & 3, fr = lane & 15, fq = lane >> 4;
;     const int K = g.K, nt = K / BK;
;     unsigned voffA[2], voffB[2];
; #pragma unroll
;     for (int i = 0; i < 2; ++i) { int R, C; stage_rc(tid * 16 + i * 8192, R, C); const int Rb = Epi::PERM ? ((R & ~31) + perm32(R & 31)) : R;
;         voffA[i] = ABLK ? (unsigned)(((((R >> 6) * 4 + (C >> 4)) * 8 + ((R >> 4) & 3)) * 64 + ((C >> 3) & 1) * 32 + (R & 15) * 2) * 8) : (unsigned)(R * K + C) * 2u; voffB[i] = (unsigned)(Rb * K + C) * 2u; }
;     const size_t kstep = (size_t)(BK * 2);
;     const size_t hstep = (size_t)HALF * K * 2;
;     const size_t kstepA = ABLK ? (size_t)32768 : kstep, hstepA = ABLK ? (size_t)2048 : hstep;
;     const size_t tstep = 2 * hstep;
;     const unsigned ldsw = (unsigned)wid * 1024u;
;     const int aoff = lds_byte(wr * 64 + fr, fq * 8), boff = lds_byte(wc * 32 + fr, fq * 8);
;     ...
;     Unit cur, nxt; int ui = 0;
;     if (!S.next(0, cur)) return;
;     f32x4 acc[2][2][4][2];
; #pragma unroll
;     for (int a = 0; a < 2; ++a)
; #pragma unroll
;         for (int b = 0; b < 2; ++b)
; #pragma unroll
;             for (int m = 0; m < 4; ++m)
; #pragma unroll
;                 for (int n = 0; n < 2; ++n) acc[a][b][m][n] = (f32x4){0.f, 0.f, 0.f, 0.f};
;     bf16x8 At[4][2], B0[2][2], B1[2][2];
;     const char* cA = (const char*)g.A + (size_t)cur.pm * tstep; const char* cB = (const char*)g.Bt + (size_t)cur.pn * tstep;
;     S.a_ready(cur);
;     if constexpr (SP2) {
;         PG8_STAGE(PG8_SB(0, 0), cB, voffB); PG8_STAGE(PG8_SB(0, 1), cB + hstep, voffB); PG8_STAGE(PG8_SA(0, 0), cA, voffA); PG8_STAGE(PG8_SA(0, 1), cA + hstepA, voffA);
;         if (wr == 1) PG8_BAR;
.LBB0_421:
	s_andn2_b64 vcc, exec, s[4:5]
	s_cbranch_vccnz .LBB0_488
	v_readlane_b32 s6, v253, 23
	v_mov_b32_e32 v1, v0
	s_mov_b64 s[4:5], s[66:67]
	s_and_b32 s11, s2, 8
	s_cmp_eq_u32 s11, 0
	s_cbranch_scc1 .Lstag_0
	s_sleep 40
.Lstag_0:
	v_mov_b32_e32 v12, v0
	v_readlane_b32 s7, v253, 24
	s_andn2_b64 vcc, exec, s[6:7]
	v_readfirstlane_b32 s50, v12
	s_cbranch_vccnz .LBB0_438
	v_lshlrev_b32_e32 v1, 4, v12
	v_add_u32_e32 v2, 0x2000, v1
	v_ashrrev_i32_e32 v4, 31, v2
	v_lshrrev_b32_e32 v4, 22, v4
	v_add_u32_e32 v4, v2, v4
	v_ashrrev_i32_e32 v13, 10, v4
	v_mul_i32_i24_e32 v4, 0x400, v13
	v_sub_u32_e32 v2, v2, v4
	v_lshrrev_b32_e32 v4, 4, v2
	v_bitop3_b32 v2, v4, v2, 32 bitop3:0x6c
	v_ashrrev_i32_e32 v4, 31, v2
	v_lshrrev_b32_e32 v4, 26, v4
	v_add_u32_e32 v4, v2, v4
	s_waitcnt lgkmcnt(0)
	v_lshlrev_b32_e32 v5, 3, v13
	v_ashrrev_i32_e32 v14, 6, v4
	v_and_b32_e32 v5, -16, v5
	v_add_u32_e32 v5, v14, v5
	v_and_b32_e32 v6, 3, v14
	s_mov_b32 s18, 0x1fffe0
	v_lshrrev_b32_e32 v7, 2, v5
	v_lshlrev_b32_e32 v8, 1, v5
	v_and_b32_e32 v4, 0xc0, v4
	v_and_or_b32 v6, v5, s18, v6
	v_and_b32_e32 v7, 4, v7
	v_and_b32_e32 v8, 24, v8
	v_sub_u32_e32 v2, v2, v4
	v_or3_b32 v6, v6, v7, v8
	v_lshlrev_b32_e32 v7, 5, v13
	v_ashrrev_i16_sdwa v2, v244, sext(v2) dst_sel:DWORD dst_unused:UNUSED_PAD src0_sel:DWORD src1_sel:BYTE_0
	v_and_b32_e32 v7, 32, v7
	v_bfe_i32 v15, v2, 0, 16
	v_add_lshl_u32 v2, v7, v15, 1
	s_waitcnt vmcnt(0)
	v_lshl_add_u32 v152, v6, 11, v2
	v_lshl_add_u32 v154, v5, 11, v2
	v_bfe_i32 v2, v12, 27, 1
	v_lshrrev_b32_e32 v2, 22, v2
	v_add_u32_e32 v2, v1, v2
	s_load_dwordx2 s[38:39], s[4:5], 0xd0
	v_and_b32_e32 v2, 0xfffffc00, v2
	v_sub_u32_e32 v1, v1, v2
	v_lshrrev_b32_e32 v2, 4, v1
	v_ashrrev_i32_e32 v4, 31, v12
	v_readlane_b32 s4, v252, 18
	v_bitop3_b32 v1, v2, v1, 32 bitop3:0x6c
	v_lshrrev_b32_e32 v4, 26, v4
	s_mul_i32 s4, s4, 0x2d80000
	v_ashrrev_i32_e32 v2, 31, v1
	v_add_u32_e32 v4, v12, v4
	v_readlane_b32 s5, v252, 19
	s_waitcnt lgkmcnt(0)
	s_add_u32 s4, s38, s4
	v_lshrrev_b32_e32 v2, 26, v2
	v_ashrrev_i32_e32 v17, 6, v4
	s_addc_u32 s5, s39, 0
	v_add_u32_e32 v2, v1, v2
	v_lshlrev_b32_e32 v4, 3, v17
	s_add_u32 s6, s4, 0x1e00000
	v_ashrrev_i32_e32 v16, 6, v2
	v_and_b32_e32 v4, -16, v4
	s_addc_u32 s7, s5, 0
	v_add_u32_e32 v4, v16, v4
	s_add_u32 s8, s38, 0x7a00000
	v_and_b32_e32 v5, 3, v16
	v_lshrrev_b32_e32 v6, 2, v4
	v_lshlrev_b32_e32 v7, 1, v4
	v_and_b32_e32 v2, 0xc0, v2
	s_addc_u32 s9, s39, 0
	s_ashr_i32 s5, s50, 6
	v_and_or_b32 v5, v4, s18, v5
	v_and_b32_e32 v6, 4, v6
	v_and_b32_e32 v7, 24, v7
	v_sub_u32_e32 v1, v1, v2
	s_ashr_i32 s4, s50, 8
	s_lshl_b32 s17, s5, 10
	v_or3_b32 v5, v5, v6, v7
	v_lshlrev_b32_e32 v6, 5, v17
	v_ashrrev_i16_sdwa v1, v244, sext(v1) dst_sel:DWORD dst_unused:UNUSED_PAD src0_sel:DWORD src1_sel:BYTE_0
	v_readlane_b32 s18, v254, 37
	v_and_b32_e32 v6, 32, v6
	v_bfe_i32 v18, v1, 0, 16
	v_readlane_b32 s19, v254, 38
	s_add_u32 s62, s6, s18
	v_add_lshl_u32 v1, v6, v18, 1
	s_addc_u32 s63, s7, s19
	s_add_i32 s18, s17, 0
	v_lshl_add_u32 v2, v5, 11, v1
	s_add_i32 m0, s18, 0x10000
	v_lshl_add_u32 v156, v4, 11, v1
	global_load_lds_dwordx4 v2, s[62:63]
	s_add_i32 m0, s18, 0x12000
	s_add_u32 s20, s62, 0x40000
	global_load_lds_dwordx4 v152, s[62:63]
	s_addc_u32 s21, s63, 0
	s_add_i32 m0, s18, 0x14000
	v_mov_b32_e32 v153, v3
	global_load_lds_dwordx4 v2, s[20:21]
	s_add_i32 m0, s18, 0x16000
	v_mov_b32_e32 v157, v3
	global_load_lds_dwordx4 v152, s[20:21]
	v_readlane_b32 s20, v254, 35
	v_readlane_b32 s21, v254, 36
	s_add_u32 s60, s8, s20
	s_addc_u32 s61, s9, s21
	s_add_i32 s19, s18, 0x2000
	s_mov_b32 m0, s18
	s_add_u32 s22, s60, 0x40000
	global_load_lds_dwordx4 v156, s[60:61]
	s_mov_b32 m0, s19
	s_addc_u32 s23, s61, 0
	s_add_i32 s20, s18, 0x4000
	global_load_lds_dwordx4 v154, s[60:61]
	s_mov_b32 m0, s20
	s_add_i32 s21, s18, 0x6000
	global_load_lds_dwordx4 v156, s[22:23]
	s_mov_b32 m0, s21
	v_mov_b32_e32 v155, v3
	global_load_lds_dwordx4 v154, s[22:23]
	s_cmp_eq_u32 s4, 1
	v_lshl_add_u64 v[10:11], s[62:63], 0, v[2:3]
	v_lshl_add_u64 v[8:9], s[62:63], 0, v[152:153]
	v_lshl_add_u64 v[4:5], s[60:61], 0, v[156:157]
	s_cselect_b64 s[44:45], -1, 0
	s_cmp_lg_u32 s4, 1
	v_lshl_add_u64 v[6:7], s[60:61], 0, v[154:155]
	s_cbranch_scc1 .LBB0_425
	s_barrier

; #define PG8_STAGE(bufoff, gbase, voff) do { _Pragma("unroll") for (int _i = 0; _i < 2; ++_i) \
;         __builtin_amdgcn_global_load_lds((const unsigned*)((const char*)(gbase) + (voff)[_i]), (PG8_LAS unsigned*)(lds + (bufoff) + ldsw + _i * 8192), 16, 0, 0); } while (0)
; #define PG8_BAR __builtin_amdgcn_s_barrier()
; template <class Epi, class Sched, bool ALIGN_EPI = false, bool SP2 = false, bool FP8 = false, bool ABLK = false>
; __device__ __forceinline__ void gemm_phase(PG8_LAS unsigned char* lds, const Gemm g, const Sched& S, const Epi& E) {
;     int tid_ = threadIdx.x; asm volatile("" : "+v"(tid_));
;     const int tid = tid_, wid = __builtin_amdgcn_readfirstlane(tid >> 6), lane = tid & 63, wr = wid >> 2, wc = wid & 3, fr = lane & 15, fq = lane >> 4;
;     const int K = g.K, nt = K / BK;
;     unsigned voffA[2], voffB[2];
; #pragma unroll
;     for (int i = 0; i < 2; ++i) { int R, C; stage_rc(tid * 16 + i * 8192, R, C); const int Rb = Epi::PERM ? ((R & ~31) + perm32(R & 31)) : R;
;         voffA[i] = ABLK ? (unsigned)(((((R >> 6) * 4 + (C >> 4)) * 8 + ((R >> 4) & 3)) * 64 + ((C >> 3) & 1) * 32 + (R & 15) * 2) * 8) : (unsigned)(R * K + C) * 2u; voffB[i] = (unsigned)(Rb * K + C) * 2u; }
;     const size_t kstep = (size_t)(BK * 2);
;     const size_t hstep = (size_t)HALF * K * 2;
;     const size_t kstepA = ABLK ? (size_t)32768 : kstep, hstepA = ABLK ? (size_t)2048 : hstep;
;     const size_t tstep = 2 * hstep;
;     const unsigned ldsw = (unsigned)wid * 1024u;
;     const int aoff = lds_byte(wr * 64 + fr, fq * 8), boff = lds_byte(wc * 32 + fr, fq * 8);
;     ...
;     Unit cur, nxt; int ui = 0;
;     if (!S.next(0, cur)) return;
;     f32x4 acc[2][2][4][2];
; #pragma unroll
;     for (int a = 0; a < 2; ++a)
; #pragma unroll
;         for (int b = 0; b < 2; ++b)
; #pragma unroll
;             for (int m = 0; m < 4; ++m)
; #pragma unroll
;                 for (int n = 0; n < 2; ++n) acc[a][b][m][n] = (f32x4){0.f, 0.f, 0.f, 0.f};
;     bf16x8 At[4][2], B0[2][2], B1[2][2];
;     const char* cA = (const char*)g.A + (size_t)cur.pm * tstep; const char* cB = (const char*)g.Bt + (size_t)cur.pn * tstep;
;     S.a_ready(cur);
;     if constexpr (SP2) {
;         PG8_STAGE(PG8_SB(0, 0), cB, voffB); PG8_STAGE(PG8_SB(0, 1), cB + hstep, voffB); PG8_STAGE(PG8_SA(0, 0), cA, voffA); PG8_STAGE(PG8_SA(0, 1), cA + hstepA, voffA);
;         if (wr == 1) PG8_BAR;
.LBB0_490:
	s_andn2_b64 vcc, exec, s[4:5]
	v_readlane_b32 s4, v254, 25
	v_readlane_b32 s5, v254, 26
	s_nop 1
	v_cndmask_b32_e64 v1, 0, 1, s[4:5]
	v_cmp_ne_u32_e64 s[4:5], 1, v1
	s_nop 1
	v_writelane_b32 v252, s4, 25
	s_nop 1
	v_writelane_b32 v252, s5, 26
	s_cbranch_vccnz .LBB0_581
	v_readlane_b32 s6, v252, 25
	v_mov_b32_e32 v1, v0
	s_mov_b64 s[4:5], s[66:67]
	s_and_b32 s11, s2, 8
	s_cmp_eq_u32 s11, 0
	s_cbranch_scc1 .Lstag_1
	s_sleep 64
.Lstag_1:
	v_mov_b32_e32 v13, v0
	v_readlane_b32 s7, v252, 26
	s_and_b64 vcc, exec, s[6:7]
	v_readfirstlane_b32 s42, v13
	s_cbranch_vccnz .LBB0_531
	v_lshlrev_b32_e32 v1, 4, v13
	v_add_u32_e32 v2, 0x2000, v1
	v_ashrrev_i32_e32 v4, 31, v2
	v_lshrrev_b32_e32 v4, 22, v4
	v_add_u32_e32 v4, v2, v4
	v_ashrrev_i32_e32 v4, 10, v4
	s_waitcnt lgkmcnt(0)
	v_mul_i32_i24_e32 v5, 0x400, v4
	v_sub_u32_e32 v2, v2, v5
	v_lshrrev_b32_e32 v5, 4, v2
	v_bitop3_b32 v2, v5, v2, 32 bitop3:0x6c
	v_ashrrev_i32_e32 v5, 31, v2
	v_lshrrev_b32_e32 v5, 26, v5
	v_add_u32_e32 v5, v2, v5
	v_lshlrev_b32_e32 v7, 3, v4
	v_ashrrev_i32_e32 v6, 6, v5
	v_and_b32_e32 v7, -16, v7
	v_add_u32_e32 v8, v6, v7
	v_and_b32_e32 v6, 3, v6
	s_mov_b32 s18, 0x1ffffe0
	v_lshrrev_b32_e32 v7, 2, v8
	v_lshlrev_b32_e32 v9, 1, v8
	v_and_b32_e32 v5, 0xc0, v5
	v_and_or_b32 v6, v8, s18, v6
	v_and_b32_e32 v7, 4, v7
	v_and_b32_e32 v9, 24, v9
	v_lshlrev_b32_e32 v4, 5, v4
	v_sub_u32_e32 v2, v2, v5
	v_or3_b32 v6, v6, v7, v9
	s_movk_i32 s19, 0x580
	v_and_b32_e32 v4, 32, v4
	v_ashrrev_i16_sdwa v2, v244, sext(v2) dst_sel:DWORD dst_unused:UNUSED_PAD src0_sel:DWORD src1_sel:BYTE_0
	v_mul_lo_u32 v6, v6, s19
	v_add_u32_sdwa v2, v4, sext(v2) dst_sel:DWORD dst_unused:UNUSED_PAD src0_sel:DWORD src1_sel:WORD_0
	s_waitcnt vmcnt(0)
	v_add_lshl_u32 v164, v6, v2, 1
	v_lshrrev_b32_e32 v9, 4, v2
	v_lshlrev_b32_e32 v2, 5, v2
	v_and_b32_e32 v11, 0x100, v2
	v_lshlrev_b32_e32 v2, 4, v8
	v_and_b32_e32 v12, 0xf0, v2
	v_bfe_i32 v2, v13, 27, 1
	v_lshrrev_b32_e32 v2, 22, v2
	s_load_dwordx2 s[40:41], s[4:5], 0xd0
	v_add_u32_e32 v2, v1, v2
	v_and_b32_e32 v2, 0xfffffc00, v2
	v_lshlrev_b32_e32 v5, 5, v8
	v_sub_u32_e32 v1, v1, v2
	v_readlane_b32 s4, v252, 18
	v_and_b32_e32 v10, 0x600, v5
	v_lshrrev_b32_e32 v2, 4, v1
	v_ashrrev_i32_e32 v5, 31, v13
	s_mul_i32 s4, s4, 0x2d80000
	v_lshrrev_b32_e32 v4, 4, v8
	v_bitop3_b32 v1, v2, v1, 32 bitop3:0x6c
	v_lshrrev_b32_e32 v5, 26, v5
	v_readlane_b32 s5, v252, 19
	s_waitcnt lgkmcnt(0)
	s_add_u32 s4, s40, s4
	v_and_b32_e32 v4, 0xffffc, v4
	v_ashrrev_i32_e32 v2, 31, v1
	v_add_u32_e32 v5, v13, v5
	s_addc_u32 s5, s41, 0
	v_add_u32_e32 v4, v9, v4
	v_lshrrev_b32_e32 v2, 26, v2
	v_ashrrev_i32_e32 v5, 6, v5
	s_add_u32 s6, s40, 0xba00000
	v_lshl_or_b32 v4, v4, 12, v10
	v_add_u32_e32 v2, v1, v2
	v_lshlrev_b32_e32 v6, 3, v5
	s_addc_u32 s7, s41, 0
	v_or3_b32 v166, v4, v11, v12
	v_ashrrev_i32_e32 v4, 6, v2
	v_and_b32_e32 v6, -16, v6
	s_add_u32 s8, s4, 0x2900000
	v_add_u32_e32 v14, v4, v6
	s_addc_u32 s9, s5, 0
	s_ashr_i32 s5, s42, 6
	v_and_b32_e32 v4, 3, v4
	v_lshrrev_b32_e32 v6, 2, v14
	v_lshlrev_b32_e32 v7, 1, v14
	v_and_b32_e32 v2, 0xc0, v2
	s_ashr_i32 s4, s42, 8
	s_lshl_b32 s17, s5, 10
	v_and_or_b32 v4, v14, s18, v4
	v_and_b32_e32 v6, 4, v6
	v_and_b32_e32 v7, 24, v7
	v_lshlrev_b32_e32 v5, 5, v5
	v_sub_u32_e32 v1, v1, v2
	v_readlane_b32 s18, v254, 59
	v_or3_b32 v4, v4, v6, v7
	v_and_b32_e32 v5, 32, v5
	v_ashrrev_i16_sdwa v1, v244, sext(v1) dst_sel:DWORD dst_unused:UNUSED_PAD src0_sel:DWORD src1_sel:BYTE_0
	s_add_u32 s56, s8, s18
	v_readlane_b32 s18, v254, 57
	v_mul_lo_u32 v4, v4, s19
	v_add_u32_sdwa v1, v5, sext(v1) dst_sel:DWORD dst_unused:UNUSED_PAD src0_sel:DWORD src1_sel:WORD_0
	s_addc_u32 s57, s9, s18
	s_add_i32 s18, s17, 0
	v_add_lshl_u32 v2, v4, v1, 1
	s_add_i32 m0, s18, 0x10000
	v_lshrrev_b32_e32 v4, 4, v14
	global_load_lds_dwordx4 v2, s[56:57]
	s_add_i32 m0, s18, 0x12000
	s_add_u32 s20, s56, 0x58000
	v_lshrrev_b32_e32 v15, 4, v1
	v_and_b32_e32 v4, 0xffffc, v4
	v_lshlrev_b32_e32 v5, 5, v14
	v_lshlrev_b32_e32 v1, 5, v1
	global_load_lds_dwordx4 v164, s[56:57]
	s_addc_u32 s21, s57, 0
	s_add_i32 m0, s18, 0x14000
	v_add_u32_e32 v4, v15, v4
	v_and_b32_e32 v16, 0x600, v5
	v_and_b32_e32 v17, 0x100, v1
	v_lshlrev_b32_e32 v1, 4, v14
	global_load_lds_dwordx4 v2, s[20:21]
	s_add_i32 m0, s18, 0x16000
	v_readlane_b32 s19, v254, 56
	v_lshl_or_b32 v4, v4, 12, v16
	v_and_b32_e32 v18, 0xf0, v1
	s_add_u32 s54, s6, s19
	v_readlane_b32 s19, v254, 55
	v_or3_b32 v168, v4, v17, v18
	global_load_lds_dwordx4 v164, s[20:21]
	s_addc_u32 s55, s7, s19
	v_mov_b32_e32 v169, v3
	s_mov_b32 m0, s18
	s_add_i32 s19, s18, 0x2000
	v_lshl_add_u64 v[4:5], s[54:55], 0, v[168:169]
	global_load_lds_dwordx4 v168, s[54:55]
	v_mov_b32_e32 v167, v3
	s_mov_b32 m0, s19
	s_add_i32 s20, s18, 0x4000
	v_lshl_add_u64 v[6:7], s[54:55], 0, v[166:167]
	global_load_lds_dwordx4 v166, s[54:55]
	v_lshl_add_u64 v[4:5], v[4:5], 0, s[24:25]
	s_mov_b32 m0, s20
	s_add_i32 s21, s18, 0x6000
	global_load_lds_dwordx4 v[4:5], off
	v_lshl_add_u64 v[4:5], v[6:7], 0, s[24:25]
	s_mov_b32 m0, s21
	v_mov_b32_e32 v165, v3
	global_load_lds_dwordx4 v[4:5], off
	s_cmp_eq_u32 s4, 1
	v_lshl_add_u64 v[4:5], s[56:57], 0, v[2:3]
	s_cselect_b64 s[38:39], -1, 0
	s_cmp_lg_u32 s4, 1
	v_lshl_add_u64 v[6:7], s[56:57], 0, v[164:165]
	s_cbranch_scc1 .LBB0_494
	s_barrier

; #define PG8_BAR __builtin_amdgcn_s_barrier()
; template <class Epi, class Sched, bool ALIGN_EPI = false, bool SP2 = false, bool FP8 = false, bool ABLK = false>
; __device__ __forceinline__ void gemm_phase(PG8_LAS unsigned char* lds, const Gemm g, const Sched& S, const Epi& E) {
;     int tid_ = threadIdx.x; asm volatile("" : "+v"(tid_));
;     const int tid = tid_, wid = __builtin_amdgcn_readfirstlane(tid >> 6), lane = tid & 63, wr = wid >> 2, wc = wid & 3, fr = lane & 15, fq = lane >> 4;
;     const int K = g.K, nt = K / BK;
;     unsigned voffA[2], voffB[2];
; #pragma unroll
;     for (int i = 0; i < 2; ++i) { int R, C; stage_rc(tid * 16 + i * 8192, R, C); const int Rb = Epi::PERM ? ((R & ~31) + perm32(R & 31)) : R;
;         voffA[i] = ABLK ? (unsigned)(((((R >> 6) * 4 + (C >> 4)) * 8 + ((R >> 4) & 3)) * 64 + ((C >> 3) & 1) * 32 + (R & 15) * 2) * 8) : (unsigned)(R * K + C) * 2u; voffB[i] = (unsigned)(Rb * K + C) * 2u; }
;     const size_t kstep = (size_t)(BK * 2);
;     const size_t hstep = (size_t)HALF * K * 2;
;     const size_t kstepA = ABLK ? (size_t)32768 : kstep, hstepA = ABLK ? (size_t)2048 : hstep;
;     const size_t tstep = 2 * hstep;
;     const unsigned ldsw = (unsigned)wid * 1024u;
;     const int aoff = lds_byte(wr * 64 + fr, fq * 8), boff = lds_byte(wc * 32 + fr, fq * 8);
;     ...
;     Unit cur, nxt; int ui = 0;
;     if (!S.next(0, cur)) return;
;     f32x4 acc[2][2][4][2];
; #pragma unroll
;     for (int a = 0; a < 2; ++a)
; #pragma unroll
;         for (int b = 0; b < 2; ++b)
; #pragma unroll
;             for (int m = 0; m < 4; ++m)
; #pragma unroll
;                 for (int n = 0; n < 2; ++n) acc[a][b][m][n] = (f32x4){0.f, 0.f, 0.f, 0.f};
;     bf16x8 At[4][2], B0[2][2], B1[2][2];
;     const char* cA = (const char*)g.A + (size_t)cur.pm * tstep; const char* cB = (const char*)g.Bt + (size_t)cur.pn * tstep;
;     S.a_ready(cur);
;     if constexpr (SP2) {
;         PG8_STAGE(PG8_SB(0, 0), cB, voffB); PG8_STAGE(PG8_SB(0, 1), cB + hstep, voffB); PG8_STAGE(PG8_SA(0, 0), cA, voffA); PG8_STAGE(PG8_SA(0, 1), cA + hstepA, voffA);
;         if (wr == 1) PG8_BAR;
; __global__ void __launch_bounds__(NWAVES * 64, 2) mk_fwd(Args args) {
;     ...
;         if (EN(4) && IN(pb + 2)) { PHASE_BEGIN(); unsigned char* wl = ws + WS_W + (size_t)l * W_LAYER;
.LBB0_583:
	s_andn2_b64 vcc, exec, s[4:5]
	v_writelane_b32 v252, s89, 27
	s_cbranch_vccnz .LBB0_936
	v_mov_b32_e32 v1, v0
	s_mov_b64 s[4:5], s[66:67]
	s_and_b32 s11, s2, 8
	s_cmp_eq_u32 s11, 0
	s_cbranch_scc1 .Lstag_2
	s_sleep 127
.Lstag_2:
	v_mov_b32_e32 v18, v0
	s_cmp_ge_i32 s2, s46
	s_nop 0
	v_readfirstlane_b32 s21, v18
	s_cbranch_scc1 .LBB0_886
	v_lshlrev_b32_e32 v1, 4, v18
	v_add_u32_e32 v2, 0x2000, v1
	v_ashrrev_i32_e32 v4, 31, v2
	v_lshrrev_b32_e32 v4, 22, v4
	v_add_u32_e32 v4, v2, v4
	v_ashrrev_i32_e32 v12, 10, v4
	v_mul_i32_i24_e32 v4, 0x400, v12
	v_sub_u32_e32 v2, v2, v4
	s_load_dwordx2 s[38:39], s[4:5], 0xd0
	v_readlane_b32 s4, v252, 18
	v_lshrrev_b32_e32 v4, 4, v2
	s_mul_i32 s4, s4, 0x2d80000
	v_bitop3_b32 v2, v4, v2, 32 bitop3:0x6c
	v_readlane_b32 s5, v252, 19
	s_add_i32 s4, s4, 0x2e80000
	v_ashrrev_i32_e32 v4, 31, v2
	s_lshr_b32 s6, s4, 19
	v_readlane_b32 s4, v254, 27
	s_ashr_i32 s5, s21, 6
	v_readlane_b32 s8, v254, 40
	v_lshrrev_b32_e32 v4, 26, v4
	s_add_i32 s17, s6, s4
	s_ashr_i32 s4, s21, 8
	s_lshl_b32 s7, s5, 10
	v_readlane_b32 s9, v254, 41
	v_add_u32_e32 v4, v2, v4
	s_waitcnt lgkmcnt(0)
	v_lshlrev_b32_e32 v5, 3, v12
	s_and_b64 s[8:9], s[8:9], exec
	v_ashrrev_i32_e32 v13, 6, v4
	v_and_b32_e32 v5, -16, v5
	v_readlane_b32 s8, v254, 39
	v_add_u32_e32 v5, v13, v5
	s_cselect_b32 s72, s17, s8
	v_and_b32_e32 v6, 3, v13
	s_mov_b32 s8, 0x1fffe0
	v_lshrrev_b32_e32 v7, 2, v5
	v_lshlrev_b32_e32 v8, 1, v5
	v_and_b32_e32 v4, 0xc0, v4
	v_and_or_b32 v6, v5, s8, v6
	v_and_b32_e32 v7, 4, v7
	v_and_b32_e32 v8, 24, v8
	v_sub_u32_e32 v2, v2, v4
	v_or3_b32 v6, v6, v7, v8
	v_lshlrev_b32_e32 v7, 5, v12
	v_ashrrev_i16_sdwa v2, v244, sext(v2) dst_sel:DWORD dst_unused:UNUSED_PAD src0_sel:DWORD src1_sel:BYTE_0
	v_and_b32_e32 v7, 32, v7
	v_bfe_i32 v14, v2, 0, 16
	v_add_lshl_u32 v2, v7, v14, 1
	s_waitcnt vmcnt(0)
	v_lshl_add_u32 v172, v6, 11, v2
	v_lshl_add_u32 v174, v5, 11, v2
	v_bfe_i32 v2, v18, 27, 1
	v_lshrrev_b32_e32 v2, 22, v2
	v_add_u32_e32 v2, v1, v2
	v_and_b32_e32 v2, 0xfffffc00, v2
	v_sub_u32_e32 v1, v1, v2
	v_lshrrev_b32_e32 v2, 4, v1
	v_ashrrev_i32_e32 v4, 31, v18
	v_bitop3_b32 v1, v2, v1, 32 bitop3:0x6c
	v_lshrrev_b32_e32 v4, 26, v4
	v_ashrrev_i32_e32 v2, 31, v1
	v_add_u32_e32 v4, v18, v4
	v_lshrrev_b32_e32 v2, 26, v2
	v_ashrrev_i32_e32 v16, 6, v4
	v_add_u32_e32 v2, v1, v2
	v_lshlrev_b32_e32 v4, 3, v16
	v_ashrrev_i32_e32 v15, 6, v2
	v_and_b32_e32 v4, -16, v4
	v_add_u32_e32 v4, v15, v4
	v_and_b32_e32 v5, 3, v15
	v_lshrrev_b32_e32 v6, 2, v4
	v_lshlrev_b32_e32 v7, 1, v4
	v_and_b32_e32 v2, 0xc0, v2
	v_and_or_b32 v5, v4, s8, v5
	v_and_b32_e32 v6, 4, v6
	v_and_b32_e32 v7, 24, v7
	v_sub_u32_e32 v1, v1, v2
	s_ashr_i32 s73, s72, 31
	v_or3_b32 v5, v5, v6, v7
	v_lshlrev_b32_e32 v6, 5, v16
	v_ashrrev_i16_sdwa v1, v244, sext(v1) dst_sel:DWORD dst_unused:UNUSED_PAD src0_sel:DWORD src1_sel:BYTE_0
	s_lshl_b64 s[8:9], s[72:73], 19
	v_and_b32_e32 v6, 32, v6
	v_bfe_i32 v17, v1, 0, 16
	s_add_u32 s44, s38, s8
	v_add_lshl_u32 v1, v6, v17, 1
	s_addc_u32 s45, s39, s9
	s_add_i32 s8, s7, 0
	v_lshl_add_u32 v2, v5, 11, v1
	s_add_i32 m0, s8, 0x10000
	v_lshl_add_u32 v176, v4, 11, v1
	global_load_lds_dwordx4 v2, s[44:45]
	s_add_i32 m0, s8, 0x12000
	s_add_u32 s18, s44, 0x40000
	global_load_lds_dwordx4 v172, s[44:45]
	s_addc_u32 s19, s45, 0
	s_add_i32 m0, s8, 0x14000
	v_mov_b32_e32 v173, v3
	global_load_lds_dwordx4 v2, s[18:19]
	s_add_i32 m0, s8, 0x16000
	v_mov_b32_e32 v177, v3
	global_load_lds_dwordx4 v172, s[18:19]
	v_readlane_b32 s18, v254, 44
	v_readlane_b32 s19, v254, 45
	s_add_u32 s42, s38, s18
	s_addc_u32 s43, s39, s19
	s_add_i32 s9, s8, 0x2000
	s_mov_b32 m0, s8
	s_add_u32 s22, s42, 0x40000
	global_load_lds_dwordx4 v176, s[42:43]
	s_mov_b32 m0, s9
	s_addc_u32 s23, s43, 0
	s_add_i32 s17, s8, 0x4000
	global_load_lds_dwordx4 v174, s[42:43]
	s_mov_b32 m0, s17
	s_add_i32 s18, s8, 0x6000
	global_load_lds_dwordx4 v176, s[22:23]
	s_mov_b32 m0, s18
	v_mov_b32_e32 v175, v3
	global_load_lds_dwordx4 v174, s[22:23]
	s_cmp_eq_u32 s4, 1
	v_lshl_add_u64 v[10:11], s[44:45], 0, v[2:3]
	v_lshl_add_u64 v[8:9], s[44:45], 0, v[172:173]
	v_lshl_add_u64 v[4:5], s[42:43], 0, v[176:177]
	s_cselect_b64 s[48:49], -1, 0
	s_cmp_lg_u32 s4, 1
	v_lshl_add_u64 v[6:7], s[42:43], 0, v[174:175]
	s_cbranch_scc1 .LBB0_587
	s_barrier

; #define PG8_STAGE(bufoff, gbase, voff) do { _Pragma("unroll") for (int _i = 0; _i < 2; ++_i) \
;         __builtin_amdgcn_global_load_lds((const unsigned*)((const char*)(gbase) + (voff)[_i]), (PG8_LAS unsigned*)(lds + (bufoff) + ldsw + _i * 8192), 16, 0, 0); } while (0)
; #define PG8_BAR __builtin_amdgcn_s_barrier()
; template <class Epi, class Sched, bool ALIGN_EPI = false, bool SP2 = false, bool FP8 = false, bool ABLK = false>
; __device__ __forceinline__ void gemm_phase(PG8_LAS unsigned char* lds, const Gemm g, const Sched& S, const Epi& E) {
;     int tid_ = threadIdx.x; asm volatile("" : "+v"(tid_));
;     const int tid = tid_, wid = __builtin_amdgcn_readfirstlane(tid >> 6), lane = tid & 63, wr = wid >> 2, wc = wid & 3, fr = lane & 15, fq = lane >> 4;
;     const int K = g.K, nt = K / BK;
;     unsigned voffA[2], voffB[2];
; #pragma unroll
;     for (int i = 0; i < 2; ++i) { int R, C; stage_rc(tid * 16 + i * 8192, R, C); const int Rb = Epi::PERM ? ((R & ~31) + perm32(R & 31)) : R;
;         voffA[i] = ABLK ? (unsigned)(((((R >> 6) * 4 + (C >> 4)) * 8 + ((R >> 4) & 3)) * 64 + ((C >> 3) & 1) * 32 + (R & 15) * 2) * 8) : (unsigned)(R * K + C) * 2u; voffB[i] = (unsigned)(Rb * K + C) * 2u; }
;     const size_t kstep = (size_t)(BK * 2);
;     const size_t hstep = (size_t)HALF * K * 2;
;     const size_t kstepA = ABLK ? (size_t)32768 : kstep, hstepA = ABLK ? (size_t)2048 : hstep;
;     const size_t tstep = 2 * hstep;
;     const unsigned ldsw = (unsigned)wid * 1024u;
;     const int aoff = lds_byte(wr * 64 + fr, fq * 8), boff = lds_byte(wc * 32 + fr, fq * 8);
;     ...
;     Unit cur, nxt; int ui = 0;
;     if (!S.next(0, cur)) return;
;     f32x4 acc[2][2][4][2];
; #pragma unroll
;     for (int a = 0; a < 2; ++a)
; #pragma unroll
;         for (int b = 0; b < 2; ++b)
; #pragma unroll
;             for (int m = 0; m < 4; ++m)
; #pragma unroll
;                 for (int n = 0; n < 2; ++n) acc[a][b][m][n] = (f32x4){0.f, 0.f, 0.f, 0.f};
;     bf16x8 At[4][2], B0[2][2], B1[2][2];
;     const char* cA = (const char*)g.A + (size_t)cur.pm * tstep; const char* cB = (const char*)g.Bt + (size_t)cur.pn * tstep;
;     S.a_ready(cur);
;     if constexpr (SP2) {
;         PG8_STAGE(PG8_SB(0, 0), cB, voffB); PG8_STAGE(PG8_SB(0, 1), cB + hstep, voffB); PG8_STAGE(PG8_SA(0, 0), cA, voffA); PG8_STAGE(PG8_SA(0, 1), cA + hstepA, voffA);
;         if (wr == 1) PG8_BAR;
.LBB0_1397:
	s_andn2_b64 vcc, exec, s[4:5]
	s_cbranch_vccnz .LBB0_1484
	v_readlane_b32 s6, v252, 25
	v_mov_b32_e32 v1, v0
	s_mov_b64 s[4:5], s[66:67]
	s_and_b32 s11, s2, 8
	s_cmp_eq_u32 s11, 0
	s_cbranch_scc1 .Lstag_3
	s_sleep 64
.Lstag_3:
	v_mov_b32_e32 v17, v0
	v_readlane_b32 s7, v252, 26
	s_and_b64 vcc, exec, s[6:7]
	v_readfirstlane_b32 s50, v17
	s_cbranch_vccnz .LBB0_1434
	v_lshlrev_b32_e32 v1, 4, v17
	v_add_u32_e32 v2, 0x2000, v1
	v_ashrrev_i32_e32 v4, 31, v2
	v_lshrrev_b32_e32 v4, 22, v4
	v_add_u32_e32 v4, v2, v4
	v_ashrrev_i32_e32 v12, 10, v4
	v_mul_i32_i24_e32 v4, 0x400, v12
	v_sub_u32_e32 v2, v2, v4
	v_lshrrev_b32_e32 v4, 4, v2
	v_bitop3_b32 v2, v4, v2, 32 bitop3:0x6c
	v_ashrrev_i32_e32 v4, 31, v2
	v_lshrrev_b32_e32 v4, 26, v4
	v_add_u32_e32 v4, v2, v4
	s_waitcnt lgkmcnt(0)
	v_lshlrev_b32_e32 v5, 3, v12
	v_ashrrev_i32_e32 v13, 6, v4
	v_and_b32_e32 v5, -16, v5
	v_add_u32_e32 v5, v13, v5
	v_and_b32_e32 v6, 3, v13
	s_mov_b32 s18, 0x1fffe0
	v_lshrrev_b32_e32 v7, 2, v5
	v_lshlrev_b32_e32 v8, 1, v5
	v_and_b32_e32 v4, 0xc0, v4
	v_and_or_b32 v6, v5, s18, v6
	v_and_b32_e32 v7, 4, v7
	v_and_b32_e32 v8, 24, v8
	v_sub_u32_e32 v2, v2, v4
	v_or3_b32 v6, v6, v7, v8
	v_lshlrev_b32_e32 v7, 5, v12
	v_ashrrev_i16_sdwa v2, v244, sext(v2) dst_sel:DWORD dst_unused:UNUSED_PAD src0_sel:DWORD src1_sel:BYTE_0
	v_and_b32_e32 v7, 32, v7
	v_bfe_i32 v14, v2, 0, 16
	v_add_lshl_u32 v2, v7, v14, 1
	s_waitcnt vmcnt(0)
	v_lshl_add_u32 v160, v6, 11, v2
	v_lshl_add_u32 v162, v5, 11, v2
	v_bfe_i32 v2, v17, 27, 1
	v_lshrrev_b32_e32 v2, 22, v2
	v_add_u32_e32 v2, v1, v2
	s_load_dwordx2 s[40:41], s[4:5], 0xd0
	v_and_b32_e32 v2, 0xfffffc00, v2
	v_sub_u32_e32 v1, v1, v2
	v_lshrrev_b32_e32 v2, 4, v1
	v_ashrrev_i32_e32 v4, 31, v17
	v_readlane_b32 s4, v252, 18
	v_bitop3_b32 v1, v2, v1, 32 bitop3:0x6c
	v_lshrrev_b32_e32 v4, 26, v4
	s_mul_i32 s4, s4, 0x2d80000
	v_ashrrev_i32_e32 v2, 31, v1
	v_add_u32_e32 v4, v17, v4
	v_readlane_b32 s5, v252, 19
	s_waitcnt lgkmcnt(0)
	s_add_u32 s4, s40, s4
	v_lshrrev_b32_e32 v2, 26, v2
	v_ashrrev_i32_e32 v16, 6, v4
	s_addc_u32 s5, s41, 0
	v_add_u32_e32 v2, v1, v2
	v_lshlrev_b32_e32 v4, 3, v16
	s_add_u32 s6, s40, 0x15f00000
	v_ashrrev_i32_e32 v15, 6, v2
	v_and_b32_e32 v4, -16, v4
	s_addc_u32 s7, s41, 0
	v_add_u32_e32 v4, v15, v4
	s_add_u32 s8, s4, 0x3500000
	v_and_b32_e32 v5, 3, v15
	v_lshrrev_b32_e32 v6, 2, v4
	v_lshlrev_b32_e32 v7, 1, v4
	v_and_b32_e32 v2, 0xc0, v2
	s_addc_u32 s9, s5, 0
	s_ashr_i32 s5, s50, 6
	v_and_or_b32 v5, v4, s18, v5
	v_and_b32_e32 v6, 4, v6
	v_and_b32_e32 v7, 24, v7
	v_sub_u32_e32 v1, v1, v2
	s_ashr_i32 s4, s50, 8
	s_lshl_b32 s17, s5, 10
	v_or3_b32 v5, v5, v6, v7
	v_lshlrev_b32_e32 v6, 5, v16
	v_ashrrev_i16_sdwa v1, v244, sext(v1) dst_sel:DWORD dst_unused:UNUSED_PAD src0_sel:DWORD src1_sel:BYTE_0
	v_readlane_b32 s18, v254, 51
	v_and_b32_e32 v6, 32, v6
	v_bfe_i32 v18, v1, 0, 16
	v_readlane_b32 s19, v254, 52
	s_add_u32 s60, s8, s18
	v_add_lshl_u32 v1, v6, v18, 1
	s_addc_u32 s61, s9, s19
	s_add_i32 s18, s17, 0
	v_lshl_add_u32 v2, v5, 11, v1
	s_add_i32 m0, s18, 0x10000
	v_lshl_add_u32 v164, v4, 11, v1
	global_load_lds_dwordx4 v2, s[60:61]
	s_add_i32 m0, s18, 0x12000
	s_add_u32 s20, s60, 0x40000
	global_load_lds_dwordx4 v160, s[60:61]
	s_addc_u32 s21, s61, 0
	s_add_i32 m0, s18, 0x14000
	v_mov_b32_e32 v161, v3
	global_load_lds_dwordx4 v2, s[20:21]
	s_add_i32 m0, s18, 0x16000
	v_mov_b32_e32 v165, v3
	global_load_lds_dwordx4 v160, s[20:21]
	v_readlane_b32 s20, v252, 10
	v_readlane_b32 s21, v252, 11
	s_add_u32 s42, s6, s20
	s_addc_u32 s43, s7, s21
	s_add_i32 s19, s18, 0x2000
	s_mov_b32 m0, s18
	s_add_u32 s22, s42, 0x40000
	global_load_lds_dwordx4 v164, s[42:43]
	s_mov_b32 m0, s19
	s_addc_u32 s23, s43, 0
	s_add_i32 s20, s18, 0x4000
	global_load_lds_dwordx4 v162, s[42:43]
	s_mov_b32 m0, s20
	s_add_i32 s21, s18, 0x6000
	global_load_lds_dwordx4 v164, s[22:23]
	s_mov_b32 m0, s21
	v_mov_b32_e32 v163, v3
	global_load_lds_dwordx4 v162, s[22:23]
	s_cmp_eq_u32 s4, 1
	v_lshl_add_u64 v[10:11], s[60:61], 0, v[2:3]
	v_lshl_add_u64 v[8:9], s[60:61], 0, v[160:161]
	v_lshl_add_u64 v[4:5], s[42:43], 0, v[164:165]
	s_cselect_b64 s[38:39], -1, 0
	s_cmp_lg_u32 s4, 1
	v_lshl_add_u64 v[6:7], s[42:43], 0, v[162:163]
	s_cbranch_scc1 .LBB0_1401
	s_barrier

; template <class Epi, class Sched, bool ALIGN_EPI = false, bool SP2 = false, bool FP8 = false, bool ABLK = false>
; __device__ __forceinline__ void gemm_phase(PG8_LAS unsigned char* lds, const Gemm g, const Sched& S, const Epi& E) {
;     int tid_ = threadIdx.x; asm volatile("" : "+v"(tid_));
;     const int tid = tid_, wid = __builtin_amdgcn_readfirstlane(tid >> 6), lane = tid & 63, wr = wid >> 2, wc = wid & 3, fr = lane & 15, fq = lane >> 4;
;     const int K = g.K, nt = K / BK;
;     unsigned voffA[2], voffB[2];
; #pragma unroll
;     for (int i = 0; i < 2; ++i) { int R, C; stage_rc(tid * 16 + i * 8192, R, C); const int Rb = Epi::PERM ? ((R & ~31) + perm32(R & 31)) : R;
;         voffA[i] = ABLK ? (unsigned)(((((R >> 6) * 4 + (C >> 4)) * 8 + ((R >> 4) & 3)) * 64 + ((C >> 3) & 1) * 32 + (R & 15) * 2) * 8) : (unsigned)(R * K + C) * 2u; voffB[i] = (unsigned)(Rb * K + C) * 2u; }
;     const size_t kstep = (size_t)(BK * 2);
;     const size_t hstep = (size_t)HALF * K * 2;
;     const size_t kstepA = ABLK ? (size_t)32768 : kstep, hstepA = ABLK ? (size_t)2048 : hstep;
;     const size_t tstep = 2 * hstep;
;     const unsigned ldsw = (unsigned)wid * 1024u;
;     const int aoff = lds_byte(wr * 64 + fr, fq * 8), boff = lds_byte(wc * 32 + fr, fq * 8);
;     ...
;     Unit cur, nxt; int ui = 0;
;     if (!S.next(0, cur)) return;
;     f32x4 acc[2][2][4][2];
; #pragma unroll
;     for (int a = 0; a < 2; ++a)
; #pragma unroll
;         for (int b = 0; b < 2; ++b)
; #pragma unroll
;             for (int m = 0; m < 4; ++m)
; #pragma unroll
;                 for (int n = 0; n < 2; ++n) acc[a][b][m][n] = (f32x4){0.f, 0.f, 0.f, 0.f};
;     bf16x8 At[4][2], B0[2][2], B1[2][2];
;     const char* cA = (const char*)g.A + (size_t)cur.pm * tstep; const char* cB = (const char*)g.Bt + (size_t)cur.pn * tstep;
;     S.a_ready(cur);
;     if constexpr (SP2) {
;         PG8_STAGE(PG8_SB(0, 0), cB, voffB); PG8_STAGE(PG8_SB(0, 1), cB + hstep, voffB); PG8_STAGE(PG8_SA(0, 0), cA, voffA); PG8_STAGE(PG8_SA(0, 1), cA + hstepA, voffA);
;         if (wr == 1) PG8_BAR;
; __global__ void __launch_bounds__(NWAVES * 64, 2) mk_fwd(Args args) {
;     ...
;         if (EN(7) && IN(pb + 6)) { PHASE_BEGIN(); unsigned char* wl = ws + WS_W + (size_t)l * W_LAYER;
;             pg8::Gemm g{(const bf16*)(ws + WS_X8), (const bf16*)(wl + WO_Q), M, D, D / 2}; pg8::StaticOrder S; S.init(M, D, F.G, (int)blockIdx.x);
.LBB0_1484:
	v_readlane_b32 s6, v253, 3
	v_readlane_b32 s7, v253, 4
	s_cmp_gt_i32 s6, s17
	s_cselect_b64 s[4:5], -1, 0
	s_cmp_ge_i32 s17, s7
	s_cselect_b64 s[6:7], -1, 0
	s_or_b64 s[4:5], s[4:5], s[6:7]
	s_and_b64 vcc, exec, s[4:5]
	s_cbranch_vccnz .LBB0_1571
	v_readlane_b32 s6, v252, 25
	v_mov_b32_e32 v1, v0
	s_mov_b64 s[4:5], s[66:67]
	s_and_b32 s11, s2, 8
	s_cmp_eq_u32 s11, 0
	s_cbranch_scc1 .Lstag_4
	s_sleep 64
.Lstag_4:
	v_mov_b32_e32 v17, v0
	v_readlane_b32 s7, v252, 26
	s_and_b64 vcc, exec, s[6:7]
	v_readfirstlane_b32 s46, v17
	s_cbranch_vccnz .LBB0_1505
	v_lshlrev_b32_e32 v1, 4, v17
	v_add_u32_e32 v2, 0x2000, v1
	v_ashrrev_i32_e32 v4, 31, v2
	v_lshrrev_b32_e32 v4, 22, v4
	v_add_u32_e32 v4, v2, v4
	v_ashrrev_i32_e32 v12, 10, v4
	v_mul_i32_i24_e32 v4, 0x400, v12
	v_sub_u32_e32 v2, v2, v4
	v_lshrrev_b32_e32 v4, 4, v2
	v_bitop3_b32 v2, v4, v2, 32 bitop3:0x6c
	v_ashrrev_i32_e32 v4, 31, v2
	v_lshrrev_b32_e32 v4, 26, v4
	v_add_u32_e32 v4, v2, v4
	s_waitcnt lgkmcnt(0)
	v_lshlrev_b32_e32 v5, 3, v12
	v_ashrrev_i32_e32 v13, 6, v4
	v_and_b32_e32 v5, -16, v5
	v_add_u32_e32 v5, v13, v5
	v_and_b32_e32 v6, 3, v13
	s_mov_b32 s18, 0x3fffe0
	v_lshrrev_b32_e32 v7, 2, v5
	v_lshlrev_b32_e32 v8, 1, v5
	v_and_b32_e32 v4, 0xc0, v4
	v_and_or_b32 v6, v5, s18, v6
	v_and_b32_e32 v7, 4, v7
	v_and_b32_e32 v8, 24, v8
	v_sub_u32_e32 v2, v2, v4
	v_or3_b32 v6, v6, v7, v8
	v_lshlrev_b32_e32 v7, 5, v12
	v_ashrrev_i16_sdwa v2, v244, sext(v2) dst_sel:DWORD dst_unused:UNUSED_PAD src0_sel:DWORD src1_sel:BYTE_0
	v_and_b32_e32 v7, 32, v7
	v_bfe_i32 v14, v2, 0, 16
	v_add_lshl_u32 v2, v7, v14, 1
	s_waitcnt vmcnt(0)
	v_lshl_add_u32 v164, v6, 10, v2
	v_lshl_add_u32 v166, v5, 10, v2
	v_bfe_i32 v2, v17, 27, 1
	v_lshrrev_b32_e32 v2, 22, v2
	v_add_u32_e32 v2, v1, v2
	s_load_dwordx2 s[40:41], s[4:5], 0xd0
	v_and_b32_e32 v2, 0xfffffc00, v2
	v_sub_u32_e32 v1, v1, v2
	v_lshrrev_b32_e32 v2, 4, v1
	v_ashrrev_i32_e32 v4, 31, v17
	v_readlane_b32 s4, v252, 18
	v_bitop3_b32 v1, v2, v1, 32 bitop3:0x6c
	v_lshrrev_b32_e32 v4, 26, v4
	s_mul_i32 s4, s4, 0x2d80000
	v_ashrrev_i32_e32 v2, 31, v1
	v_add_u32_e32 v4, v17, v4
	v_readlane_b32 s5, v252, 19
	s_waitcnt lgkmcnt(0)
	s_add_u32 s4, s40, s4
	v_lshrrev_b32_e32 v2, 26, v2
	v_ashrrev_i32_e32 v16, 6, v4
	s_addc_u32 s5, s41, 0
	v_add_u32_e32 v2, v1, v2
	v_lshlrev_b32_e32 v4, 3, v16
	s_add_u32 s6, s40, 0x11a00000
	v_ashrrev_i32_e32 v15, 6, v2
	v_and_b32_e32 v4, -16, v4
	s_addc_u32 s7, s41, 0
	v_add_u32_e32 v4, v15, v4
	s_add_u32 s8, s4, 0x3700000
	v_and_b32_e32 v5, 3, v15
	v_lshrrev_b32_e32 v6, 2, v4
	v_lshlrev_b32_e32 v7, 1, v4
	v_and_b32_e32 v2, 0xc0, v2
	s_addc_u32 s9, s5, 0
	s_ashr_i32 s4, s46, 6
	v_and_or_b32 v5, v4, s18, v5
	v_and_b32_e32 v6, 4, v6
	v_and_b32_e32 v7, 24, v7
	v_sub_u32_e32 v1, v1, v2
	s_ashr_i32 s5, s46, 8
	s_lshl_b32 s17, s4, 10
	v_or3_b32 v5, v5, v6, v7
	v_lshlrev_b32_e32 v6, 5, v16
	v_ashrrev_i16_sdwa v1, v244, sext(v1) dst_sel:DWORD dst_unused:UNUSED_PAD src0_sel:DWORD src1_sel:BYTE_0
	v_readlane_b32 s18, v254, 49
	v_and_b32_e32 v6, 32, v6
	v_bfe_i32 v18, v1, 0, 16
	v_readlane_b32 s19, v254, 50
	s_add_u32 s58, s8, s18
	v_add_lshl_u32 v1, v6, v18, 1
	s_addc_u32 s59, s9, s19
	s_add_i32 s18, s17, 0
	v_lshl_add_u32 v2, v5, 10, v1
	s_add_i32 m0, s18, 0x10000
	v_lshl_add_u32 v168, v4, 10, v1
	global_load_lds_dwordx4 v2, s[58:59]
	s_add_i32 m0, s18, 0x12000
	s_add_u32 s20, s58, 0x20000
	global_load_lds_dwordx4 v164, s[58:59]
	s_addc_u32 s21, s59, 0
	s_add_i32 m0, s18, 0x14000
	v_mov_b32_e32 v165, v3
	global_load_lds_dwordx4 v2, s[20:21]
	s_add_i32 m0, s18, 0x16000
	v_mov_b32_e32 v169, v3
	global_load_lds_dwordx4 v164, s[20:21]
	v_readlane_b32 s20, v252, 2
	v_readlane_b32 s21, v252, 3
	s_add_u32 s56, s6, s20
	s_addc_u32 s57, s7, s21
	s_add_i32 s19, s18, 0x2000
	s_mov_b32 m0, s18
	s_add_u32 s22, s56, 0x20000
	global_load_lds_dwordx4 v168, s[56:57]
	s_mov_b32 m0, s19
	s_addc_u32 s23, s57, 0
	s_add_i32 s20, s18, 0x4000
	global_load_lds_dwordx4 v166, s[56:57]
	s_mov_b32 m0, s20
	s_add_i32 s21, s18, 0x6000
	global_load_lds_dwordx4 v168, s[22:23]
	s_mov_b32 m0, s21
	v_mov_b32_e32 v167, v3
	global_load_lds_dwordx4 v166, s[22:23]
	s_cmp_eq_u32 s5, 1
	v_lshl_add_u64 v[10:11], s[58:59], 0, v[2:3]
	v_lshl_add_u64 v[8:9], s[58:59], 0, v[164:165]
	v_lshl_add_u64 v[4:5], s[56:57], 0, v[168:169]
	s_cselect_b64 s[38:39], -1, 0
	s_cmp_lg_u32 s5, 1
	v_lshl_add_u64 v[6:7], s[56:57], 0, v[166:167]
	s_cbranch_scc1 .LBB0_1488
	s_barrier

; #define PG8_STAGE(bufoff, gbase, voff) do { _Pragma("unroll") for (int _i = 0; _i < 2; ++_i) \
;         __builtin_amdgcn_global_load_lds((const unsigned*)((const char*)(gbase) + (voff)[_i]), (PG8_LAS unsigned*)(lds + (bufoff) + ldsw + _i * 8192), 16, 0, 0); } while (0)
; #define PG8_BAR __builtin_amdgcn_s_barrier()
; template <class Epi, class Sched, bool ALIGN_EPI = false, bool SP2 = false, bool FP8 = false, bool ABLK = false>
; __device__ __forceinline__ void gemm_phase(PG8_LAS unsigned char* lds, const Gemm g, const Sched& S, const Epi& E) {
;     int tid_ = threadIdx.x; asm volatile("" : "+v"(tid_));
;     const int tid = tid_, wid = __builtin_amdgcn_readfirstlane(tid >> 6), lane = tid & 63, wr = wid >> 2, wc = wid & 3, fr = lane & 15, fq = lane >> 4;
;     const int K = g.K, nt = K / BK;
;     unsigned voffA[2], voffB[2];
; #pragma unroll
;     for (int i = 0; i < 2; ++i) { int R, C; stage_rc(tid * 16 + i * 8192, R, C); const int Rb = Epi::PERM ? ((R & ~31) + perm32(R & 31)) : R;
;         voffA[i] = ABLK ? (unsigned)(((((R >> 6) * 4 + (C >> 4)) * 8 + ((R >> 4) & 3)) * 64 + ((C >> 3) & 1) * 32 + (R & 15) * 2) * 8) : (unsigned)(R * K + C) * 2u; voffB[i] = (unsigned)(Rb * K + C) * 2u; }
;     const size_t kstep = (size_t)(BK * 2);
;     const size_t hstep = (size_t)HALF * K * 2;
;     const size_t kstepA = ABLK ? (size_t)32768 : kstep, hstepA = ABLK ? (size_t)2048 : hstep;
;     const size_t tstep = 2 * hstep;
;     const unsigned ldsw = (unsigned)wid * 1024u;
;     const int aoff = lds_byte(wr * 64 + fr, fq * 8), boff = lds_byte(wc * 32 + fr, fq * 8);
;     ...
;     Unit cur, nxt; int ui = 0;
;     if (!S.next(0, cur)) return;
;     f32x4 acc[2][2][4][2];
; #pragma unroll
;     for (int a = 0; a < 2; ++a)
; #pragma unroll
;         for (int b = 0; b < 2; ++b)
; #pragma unroll
;             for (int m = 0; m < 4; ++m)
; #pragma unroll
;                 for (int n = 0; n < 2; ++n) acc[a][b][m][n] = (f32x4){0.f, 0.f, 0.f, 0.f};
;     bf16x8 At[4][2], B0[2][2], B1[2][2];
;     const char* cA = (const char*)g.A + (size_t)cur.pm * tstep; const char* cB = (const char*)g.Bt + (size_t)cur.pn * tstep;
;     S.a_ready(cur);
;     if constexpr (SP2) {
;         PG8_STAGE(PG8_SB(0, 0), cB, voffB); PG8_STAGE(PG8_SB(0, 1), cB + hstep, voffB); PG8_STAGE(PG8_SA(0, 0), cA, voffA); PG8_STAGE(PG8_SA(0, 1), cA + hstepA, voffA);
;         if (wr == 1) PG8_BAR;
.Lstag_5:
	v_mov_b32_e32 v17, v0
	v_readlane_b32 s7, v252, 26
	s_and_b64 vcc, exec, s[6:7]
	v_readfirstlane_b32 s50, v17
	s_cbranch_vccnz .LBB0_1610
	v_lshlrev_b32_e32 v1, 4, v17
	v_add_u32_e32 v2, 0x2000, v1
	v_ashrrev_i32_e32 v4, 31, v2
	v_lshrrev_b32_e32 v4, 22, v4
	v_add_u32_e32 v4, v2, v4
	v_ashrrev_i32_e32 v12, 10, v4
	v_mul_i32_i24_e32 v4, 0x400, v12
	v_sub_u32_e32 v2, v2, v4
	v_lshrrev_b32_e32 v4, 4, v2
	v_bitop3_b32 v2, v4, v2, 32 bitop3:0x6c
	v_ashrrev_i32_e32 v4, 31, v2
	v_lshrrev_b32_e32 v4, 26, v4
	v_add_u32_e32 v4, v2, v4
	s_waitcnt lgkmcnt(0)
	v_lshlrev_b32_e32 v5, 3, v12
	v_ashrrev_i32_e32 v13, 6, v4
	v_and_b32_e32 v5, -16, v5
	v_add_u32_e32 v5, v13, v5
	v_and_b32_e32 v6, 3, v13
	s_mov_b32 s18, 0x3fffe0
	v_lshrrev_b32_e32 v7, 2, v5
	v_lshlrev_b32_e32 v8, 1, v5
	v_and_b32_e32 v4, 0xc0, v4
	v_and_or_b32 v6, v5, s18, v6
	v_and_b32_e32 v7, 4, v7
	v_and_b32_e32 v8, 24, v8
	v_sub_u32_e32 v2, v2, v4
	v_or3_b32 v6, v6, v7, v8
	v_lshlrev_b32_e32 v7, 5, v12
	v_ashrrev_i16_sdwa v2, v244, sext(v2) dst_sel:DWORD dst_unused:UNUSED_PAD src0_sel:DWORD src1_sel:BYTE_0
	v_and_b32_e32 v7, 32, v7
	v_bfe_i32 v14, v2, 0, 16
	v_add_lshl_u32 v2, v7, v14, 1
	s_waitcnt vmcnt(0)
	v_lshl_add_u32 v164, v6, 10, v2
	v_lshl_add_u32 v166, v5, 10, v2
	v_bfe_i32 v2, v17, 27, 1
	v_lshrrev_b32_e32 v2, 22, v2
	v_add_u32_e32 v2, v1, v2
	s_load_dwordx2 s[40:41], s[4:5], 0xd0
	v_and_b32_e32 v2, 0xfffffc00, v2
	v_sub_u32_e32 v1, v1, v2
	v_lshrrev_b32_e32 v2, 4, v1
	v_ashrrev_i32_e32 v4, 31, v17
	v_readlane_b32 s4, v252, 18
	v_bitop3_b32 v1, v2, v1, 32 bitop3:0x6c
	v_lshrrev_b32_e32 v4, 26, v4
	s_mul_i32 s4, s4, 0x2d80000
	v_ashrrev_i32_e32 v2, 31, v1
	v_add_u32_e32 v4, v17, v4
	v_readlane_b32 s5, v252, 19
	s_waitcnt lgkmcnt(0)
	s_add_u32 s4, s40, s4
	v_lshrrev_b32_e32 v2, 26, v2
	v_ashrrev_i32_e32 v16, 6, v4
	s_addc_u32 s5, s41, 0
	v_add_u32_e32 v2, v1, v2
	v_lshlrev_b32_e32 v4, 3, v16
	s_add_u32 s6, s40, 0xfa00000
	v_ashrrev_i32_e32 v15, 6, v2
	v_and_b32_e32 v4, -16, v4
	s_addc_u32 s7, s41, 0
	v_add_u32_e32 v4, v15, v4
	s_add_u32 s8, s4, 0x3900000
	v_and_b32_e32 v5, 3, v15
	v_lshrrev_b32_e32 v6, 2, v4
	v_lshlrev_b32_e32 v7, 1, v4
	v_and_b32_e32 v2, 0xc0, v2
	s_addc_u32 s9, s5, 0
	s_ashr_i32 s5, s50, 6
	v_and_or_b32 v5, v4, s18, v5
	v_and_b32_e32 v6, 4, v6
	v_and_b32_e32 v7, 24, v7
	v_sub_u32_e32 v1, v1, v2
	s_ashr_i32 s4, s50, 8
	s_lshl_b32 s17, s5, 10
	v_or3_b32 v5, v5, v6, v7
	v_lshlrev_b32_e32 v6, 5, v16
	v_ashrrev_i16_sdwa v1, v244, sext(v1) dst_sel:DWORD dst_unused:UNUSED_PAD src0_sel:DWORD src1_sel:BYTE_0
	v_readlane_b32 s18, v254, 49
	v_and_b32_e32 v6, 32, v6
	v_bfe_i32 v18, v1, 0, 16
	v_readlane_b32 s19, v254, 50
	s_add_u32 s60, s8, s18
	v_add_lshl_u32 v1, v6, v18, 1
	s_addc_u32 s61, s9, s19
	s_add_i32 s18, s17, 0
	v_lshl_add_u32 v2, v5, 10, v1
	s_add_i32 m0, s18, 0x10000
	v_lshl_add_u32 v168, v4, 10, v1
	global_load_lds_dwordx4 v2, s[60:61]
	s_add_i32 m0, s18, 0x12000
	s_add_u32 s20, s60, 0x20000
	global_load_lds_dwordx4 v164, s[60:61]
	s_addc_u32 s21, s61, 0
	s_add_i32 m0, s18, 0x14000
	v_mov_b32_e32 v165, v3
	global_load_lds_dwordx4 v2, s[20:21]
	s_add_i32 m0, s18, 0x16000
	v_mov_b32_e32 v169, v3
	global_load_lds_dwordx4 v164, s[20:21]
	v_readlane_b32 s20, v252, 2
	v_readlane_b32 s21, v252, 3
	s_add_u32 s42, s6, s20
	s_addc_u32 s43, s7, s21
	s_add_i32 s19, s18, 0x2000
	s_mov_b32 m0, s18
	s_add_u32 s22, s42, 0x20000
	global_load_lds_dwordx4 v168, s[42:43]
	s_mov_b32 m0, s19
	s_addc_u32 s23, s43, 0
	s_add_i32 s20, s18, 0x4000
	global_load_lds_dwordx4 v166, s[42:43]
	s_mov_b32 m0, s20
	s_add_i32 s21, s18, 0x6000
	global_load_lds_dwordx4 v168, s[22:23]
	s_mov_b32 m0, s21
	v_mov_b32_e32 v167, v3
	global_load_lds_dwordx4 v166, s[22:23]
	s_cmp_eq_u32 s4, 1
	v_lshl_add_u64 v[10:11], s[60:61], 0, v[2:3]
	v_lshl_add_u64 v[8:9], s[60:61], 0, v[164:165]
	v_lshl_add_u64 v[4:5], s[42:43], 0, v[168:169]
	s_cselect_b64 s[38:39], -1, 0
	s_cmp_lg_u32 s4, 1
	v_lshl_add_u64 v[6:7], s[42:43], 0, v[166:167]
	s_cbranch_scc1 .LBB0_1577
	s_barrier

; #define PG8_BAR __builtin_amdgcn_s_barrier()
; template <class Epi, class Sched, bool ALIGN_EPI = false, bool SP2 = false, bool FP8 = false, bool ABLK = false>
; __device__ __forceinline__ void gemm_phase(PG8_LAS unsigned char* lds, const Gemm g, const Sched& S, const Epi& E) {
;     int tid_ = threadIdx.x; asm volatile("" : "+v"(tid_));
;     const int tid = tid_, wid = __builtin_amdgcn_readfirstlane(tid >> 6), lane = tid & 63, wr = wid >> 2, wc = wid & 3, fr = lane & 15, fq = lane >> 4;
;     const int K = g.K, nt = K / BK;
;     unsigned voffA[2], voffB[2];
; #pragma unroll
;     for (int i = 0; i < 2; ++i) { int R, C; stage_rc(tid * 16 + i * 8192, R, C); const int Rb = Epi::PERM ? ((R & ~31) + perm32(R & 31)) : R;
;         voffA[i] = ABLK ? (unsigned)(((((R >> 6) * 4 + (C >> 4)) * 8 + ((R >> 4) & 3)) * 64 + ((C >> 3) & 1) * 32 + (R & 15) * 2) * 8) : (unsigned)(R * K + C) * 2u; voffB[i] = (unsigned)(Rb * K + C) * 2u; }
;     const size_t kstep = (size_t)(BK * 2);
;     const size_t hstep = (size_t)HALF * K * 2;
;     const size_t kstepA = ABLK ? (size_t)32768 : kstep, hstepA = ABLK ? (size_t)2048 : hstep;
;     const size_t tstep = 2 * hstep;
;     const unsigned ldsw = (unsigned)wid * 1024u;
;     const int aoff = lds_byte(wr * 64 + fr, fq * 8), boff = lds_byte(wc * 32 + fr, fq * 8);
;     ...
;     Unit cur, nxt; int ui = 0;
;     if (!S.next(0, cur)) return;
;     f32x4 acc[2][2][4][2];
; #pragma unroll
;     for (int a = 0; a < 2; ++a)
; #pragma unroll
;         for (int b = 0; b < 2; ++b)
; #pragma unroll
;             for (int m = 0; m < 4; ++m)
; #pragma unroll
;                 for (int n = 0; n < 2; ++n) acc[a][b][m][n] = (f32x4){0.f, 0.f, 0.f, 0.f};
;     bf16x8 At[4][2], B0[2][2], B1[2][2];
;     const char* cA = (const char*)g.A + (size_t)cur.pm * tstep; const char* cB = (const char*)g.Bt + (size_t)cur.pn * tstep;
;     S.a_ready(cur);
;     if constexpr (SP2) {
;         PG8_STAGE(PG8_SB(0, 0), cB, voffB); PG8_STAGE(PG8_SB(0, 1), cB + hstep, voffB); PG8_STAGE(PG8_SA(0, 0), cA, voffA); PG8_STAGE(PG8_SA(0, 1), cA + hstepA, voffA);
;         if (wr == 1) PG8_BAR;
; __global__ void __launch_bounds__(NWAVES * 64, 2) mk_fwd(Args args) {
;     ...
;         else if (EN(2) && IN(pb + 9)) { PHASE_BEGIN(); unsigned char* wl = ws + WS_W + (size_t)l * W_LAYER;
.LBB0_1660:
	v_readlane_b32 s6, v253, 3
	v_readlane_b32 s7, v253, 4
	s_cmp_le_i32 s6, s17
	s_cselect_b64 s[4:5], -1, 0
	s_cmp_lt_i32 s17, s7
	s_cselect_b64 s[6:7], -1, 0
	s_and_b64 s[38:39], s[4:5], s[6:7]
	v_readlane_b32 s4, v252, 23
	v_readlane_b32 s5, v252, 24
	s_and_b64 vcc, exec, s[4:5]
	s_cbranch_vccz .LBB0_1677
	s_mov_b64 s[42:43], 0
	s_and_b64 vcc, exec, s[38:39]
	s_mov_b64 s[44:45], 0
	s_cbranch_vccz .LBB0_1678
	v_mov_b32_e32 v1, v0
	s_mov_b64 s[4:5], s[66:67]
	s_and_b32 s11, s2, 8
	s_cmp_eq_u32 s11, 0
	s_cbranch_scc1 .Lstag_6
	s_sleep 40
.Lstag_6:
	s_load_dwordx2 s[46:47], s[4:5], 0xd0
	v_readlane_b32 s4, v254, 32
	v_mov_b32_e32 v10, v0
	v_readlane_b32 s5, v254, 33
	s_waitcnt lgkmcnt(0)
	s_add_u32 s6, s46, 0xba00000
	s_addc_u32 s7, s47, 0
	s_add_u32 s44, s46, 0x1c200000
	s_addc_u32 s45, s47, 0
	s_andn2_b64 vcc, exec, s[4:5]
	v_readfirstlane_b32 s4, v10
	s_cbranch_vccnz .LBB0_1696
	v_lshlrev_b32_e32 v1, 4, v10
	v_add_u32_e32 v2, 0x2000, v1
	v_ashrrev_i32_e32 v4, 31, v2
	v_lshrrev_b32_e32 v4, 22, v4
	v_add_u32_e32 v4, v2, v4
	v_ashrrev_i32_e32 v4, 10, v4
	v_mul_i32_i24_e32 v5, 0x400, v4
	v_sub_u32_e32 v2, v2, v5
	v_lshrrev_b32_e32 v5, 4, v2
	v_bitop3_b32 v2, v5, v2, 32 bitop3:0x6c
	v_ashrrev_i32_e32 v5, 31, v2
	v_lshrrev_b32_e32 v5, 26, v5
	v_add_u32_e32 v6, v2, v5
	v_lshlrev_b32_e32 v7, 3, v4
	v_ashrrev_i32_e32 v5, 6, v6
	v_and_b32_e32 v7, -16, v7
	v_add_u32_e32 v7, v5, v7
	v_and_b32_e32 v8, 3, v5
	s_mov_b32 s20, 0x3fffe0
	v_lshrrev_b32_e32 v9, 2, v7
	v_lshlrev_b32_e32 v11, 1, v7
	v_and_b32_e32 v6, 0xc0, v6
	v_and_or_b32 v8, v7, s20, v8
	v_and_b32_e32 v9, 4, v9
	v_and_b32_e32 v11, 24, v11
	v_sub_u32_e32 v2, v2, v6
	v_or3_b32 v8, v8, v9, v11
	v_lshlrev_b32_e32 v9, 5, v4
	v_ashrrev_i16_sdwa v2, v244, sext(v2) dst_sel:DWORD dst_unused:UNUSED_PAD src0_sel:DWORD src1_sel:BYTE_0
	v_and_b32_e32 v9, 32, v9
	v_bfe_i32 v6, v2, 0, 16
	v_add_lshl_u32 v2, v9, v6, 1
	s_waitcnt vmcnt(0)
	v_lshl_add_u32 v164, v8, 10, v2
	v_lshl_add_u32 v166, v7, 10, v2
	v_bfe_i32 v2, v10, 27, 1
	v_lshrrev_b32_e32 v2, 22, v2
	v_add_u32_e32 v2, v1, v2
	v_and_b32_e32 v2, 0xfffffc00, v2
	v_sub_u32_e32 v1, v1, v2
	v_lshrrev_b32_e32 v2, 4, v1
	v_ashrrev_i32_e32 v8, 31, v10
	v_bitop3_b32 v1, v2, v1, 32 bitop3:0x6c
	v_lshrrev_b32_e32 v8, 26, v8
	v_ashrrev_i32_e32 v2, 31, v1
	v_add_u32_e32 v8, v10, v8
	v_lshrrev_b32_e32 v2, 26, v2
	v_ashrrev_i32_e32 v8, 6, v8
	v_add_u32_e32 v2, v1, v2
	v_lshlrev_b32_e32 v9, 3, v8
	s_add_u32 s8, s46, 0x11a00000
	v_ashrrev_i32_e32 v7, 6, v2
	v_and_b32_e32 v9, -16, v9
	s_addc_u32 s9, s47, 0
	v_add_u32_e32 v11, v7, v9
	s_add_u32 s17, s46, 0x3b00000
	v_and_b32_e32 v9, 3, v7
	v_lshrrev_b32_e32 v12, 2, v11
	v_lshlrev_b32_e32 v13, 1, v11
	v_and_b32_e32 v2, 0xc0, v2
	s_addc_u32 s18, s47, 0
	s_ashr_i32 s40, s4, 6
	v_and_or_b32 v9, v11, s20, v9
	v_and_b32_e32 v12, 4, v12
	v_and_b32_e32 v13, 24, v13
	v_sub_u32_e32 v1, v1, v2
	s_ashr_i32 s5, s4, 8
	s_lshl_b32 s19, s40, 10
	v_or3_b32 v12, v9, v12, v13
	v_lshlrev_b32_e32 v9, 5, v8
	v_ashrrev_i16_sdwa v1, v244, sext(v1) dst_sel:DWORD dst_unused:UNUSED_PAD src0_sel:DWORD src1_sel:BYTE_0
	v_readlane_b32 s20, v254, 47
	v_and_b32_e32 v13, 32, v9
	v_bfe_i32 v9, v1, 0, 16
	v_readlane_b32 s21, v254, 48
	s_add_u32 s62, s17, s20
	v_add_lshl_u32 v1, v13, v9, 1
	s_addc_u32 s63, s18, s21
	s_add_i32 s20, s19, 0
	v_lshl_add_u32 v2, v12, 10, v1
	s_add_i32 m0, s20, 0x10000
	v_lshl_add_u32 v168, v11, 10, v1
	global_load_lds_dwordx4 v2, s[62:63]
	s_add_i32 m0, s20, 0x12000
	s_add_u32 s22, s62, 0x20000
	global_load_lds_dwordx4 v164, s[62:63]
	s_addc_u32 s23, s63, 0
	s_add_i32 m0, s20, 0x14000
	s_nop 0
	global_load_lds_dwordx4 v2, s[22:23]
	s_add_i32 m0, s20, 0x16000
	s_nop 0
	global_load_lds_dwordx4 v164, s[22:23]
	v_readlane_b32 s22, v252, 6
	v_readlane_b32 s23, v252, 7
	s_add_u32 s60, s8, s22
	s_addc_u32 s61, s9, s23
	s_add_i32 s21, s20, 0x2000
	s_mov_b32 m0, s20
	s_add_u32 s48, s60, 0x20000
	global_load_lds_dwordx4 v168, s[60:61]
	s_mov_b32 m0, s21
	s_addc_u32 s49, s61, 0
	s_add_i32 s22, s20, 0x4000
	global_load_lds_dwordx4 v166, s[60:61]
	s_mov_b32 m0, s22
	s_add_i32 s23, s20, 0x6000
	global_load_lds_dwordx4 v168, s[48:49]
	s_mov_b32 m0, s23
	s_cmp_eq_u32 s5, 1
	global_load_lds_dwordx4 v166, s[48:49]
	s_cselect_b64 s[48:49], -1, 0
	s_cmp_lg_u32 s5, 1
	s_cbranch_scc1 .LBB0_1665
	s_barrier

; #define PG8_STAGE(bufoff, gbase, voff) do { _Pragma("unroll") for (int _i = 0; _i < 2; ++_i) \
;         __builtin_amdgcn_global_load_lds((const unsigned*)((const char*)(gbase) + (voff)[_i]), (PG8_LAS unsigned*)(lds + (bufoff) + ldsw + _i * 8192), 16, 0, 0); } while (0)
; #define PG8_BAR __builtin_amdgcn_s_barrier()
; template <class Epi, class Sched, bool ALIGN_EPI = false, bool SP2 = false, bool FP8 = false, bool ABLK = false>
; __device__ __forceinline__ void gemm_phase(PG8_LAS unsigned char* lds, const Gemm g, const Sched& S, const Epi& E) {
;     int tid_ = threadIdx.x; asm volatile("" : "+v"(tid_));
;     const int tid = tid_, wid = __builtin_amdgcn_readfirstlane(tid >> 6), lane = tid & 63, wr = wid >> 2, wc = wid & 3, fr = lane & 15, fq = lane >> 4;
;     const int K = g.K, nt = K / BK;
;     unsigned voffA[2], voffB[2];
; #pragma unroll
;     for (int i = 0; i < 2; ++i) { int R, C; stage_rc(tid * 16 + i * 8192, R, C); const int Rb = Epi::PERM ? ((R & ~31) + perm32(R & 31)) : R;
;         voffA[i] = ABLK ? (unsigned)(((((R >> 6) * 4 + (C >> 4)) * 8 + ((R >> 4) & 3)) * 64 + ((C >> 3) & 1) * 32 + (R & 15) * 2) * 8) : (unsigned)(R * K + C) * 2u; voffB[i] = (unsigned)(Rb * K + C) * 2u; }
;     const size_t kstep = (size_t)(BK * 2);
;     const size_t hstep = (size_t)HALF * K * 2;
;     const size_t kstepA = ABLK ? (size_t)32768 : kstep, hstepA = ABLK ? (size_t)2048 : hstep;
;     const size_t tstep = 2 * hstep;
;     const unsigned ldsw = (unsigned)wid * 1024u;
;     const int aoff = lds_byte(wr * 64 + fr, fq * 8), boff = lds_byte(wc * 32 + fr, fq * 8);
;     ...
;     Unit cur, nxt; int ui = 0;
;     if (!S.next(0, cur)) return;
;     f32x4 acc[2][2][4][2];
; #pragma unroll
;     for (int a = 0; a < 2; ++a)
; #pragma unroll
;         for (int b = 0; b < 2; ++b)
; #pragma unroll
;             for (int m = 0; m < 4; ++m)
; #pragma unroll
;                 for (int n = 0; n < 2; ++n) acc[a][b][m][n] = (f32x4){0.f, 0.f, 0.f, 0.f};
;     bf16x8 At[4][2], B0[2][2], B1[2][2];
;     const char* cA = (const char*)g.A + (size_t)cur.pm * tstep; const char* cB = (const char*)g.Bt + (size_t)cur.pn * tstep;
;     S.a_ready(cur);
;     if constexpr (SP2) {
;         PG8_STAGE(PG8_SB(0, 0), cB, voffB); PG8_STAGE(PG8_SB(0, 1), cB + hstep, voffB); PG8_STAGE(PG8_SA(0, 0), cA, voffA); PG8_STAGE(PG8_SA(0, 1), cA + hstepA, voffA);
;         if (wr == 1) PG8_BAR;
.LBB0_1678:
	s_and_b64 vcc, exec, s[42:43]
	s_cbranch_vccz .LBB0_1811
	s_and_b64 vcc, exec, s[38:39]
	s_cbranch_vccz .LBB0_1811
	v_readlane_b32 s6, v253, 23
	v_mov_b32_e32 v1, v0
	s_mov_b64 s[4:5], s[66:67]
	s_and_b32 s11, s2, 8
	s_cmp_eq_u32 s11, 0
	s_cbranch_scc1 .Lstag_7
	s_sleep 40
.Lstag_7:
	v_mov_b32_e32 v18, v0
	v_readlane_b32 s7, v253, 24
	s_andn2_b64 vcc, exec, s[6:7]
	v_readfirstlane_b32 s46, v18
	s_cbranch_vccnz .LBB0_1716
	v_lshlrev_b32_e32 v1, 4, v18
	v_add_u32_e32 v2, 0x2000, v1
	v_ashrrev_i32_e32 v4, 31, v2
	v_lshrrev_b32_e32 v4, 22, v4
	v_add_u32_e32 v4, v2, v4
	v_ashrrev_i32_e32 v12, 10, v4
	v_mul_i32_i24_e32 v4, 0x400, v12
	v_sub_u32_e32 v2, v2, v4
	v_lshrrev_b32_e32 v4, 4, v2
	v_bitop3_b32 v2, v4, v2, 32 bitop3:0x6c
	v_ashrrev_i32_e32 v4, 31, v2
	v_lshrrev_b32_e32 v4, 26, v4
	v_add_u32_e32 v4, v2, v4
	s_waitcnt lgkmcnt(0)
	v_lshlrev_b32_e32 v5, 3, v12
	v_ashrrev_i32_e32 v13, 6, v4
	v_and_b32_e32 v5, -16, v5
	v_add_u32_e32 v5, v13, v5
	v_and_b32_e32 v6, 3, v13
	s_mov_b32 s18, 0x3fffe0
	v_lshrrev_b32_e32 v7, 2, v5
	v_lshlrev_b32_e32 v8, 1, v5
	v_and_b32_e32 v4, 0xc0, v4
	v_and_or_b32 v6, v5, s18, v6
	v_and_b32_e32 v7, 4, v7
	v_and_b32_e32 v8, 24, v8
	v_sub_u32_e32 v2, v2, v4
	v_or3_b32 v6, v6, v7, v8
	v_lshlrev_b32_e32 v7, 5, v12
	v_ashrrev_i16_sdwa v2, v244, sext(v2) dst_sel:DWORD dst_unused:UNUSED_PAD src0_sel:DWORD src1_sel:BYTE_0
	v_and_b32_e32 v7, 32, v7
	v_bfe_i32 v14, v2, 0, 16
	v_add_lshl_u32 v2, v7, v14, 1
	s_waitcnt vmcnt(0)
	v_lshl_add_u32 v164, v6, 10, v2
	v_lshl_add_u32 v166, v5, 10, v2
	v_bfe_i32 v2, v18, 27, 1
	v_lshrrev_b32_e32 v2, 22, v2
	v_add_u32_e32 v2, v1, v2
	v_and_b32_e32 v2, 0xfffffc00, v2
	v_sub_u32_e32 v1, v1, v2
	s_load_dwordx2 s[40:41], s[4:5], 0xd0
	v_lshrrev_b32_e32 v2, 4, v1
	v_ashrrev_i32_e32 v4, 31, v18
	v_bitop3_b32 v1, v2, v1, 32 bitop3:0x6c
	v_lshrrev_b32_e32 v4, 26, v4
	v_ashrrev_i32_e32 v2, 31, v1
	v_add_u32_e32 v4, v18, v4
	v_lshrrev_b32_e32 v2, 26, v2
	v_ashrrev_i32_e32 v16, 6, v4
	v_add_u32_e32 v2, v1, v2
	v_lshlrev_b32_e32 v4, 3, v16
	s_waitcnt lgkmcnt(0)
	s_add_u32 s6, s40, 0x11a00000
	v_ashrrev_i32_e32 v15, 6, v2
	v_and_b32_e32 v4, -16, v4
	s_addc_u32 s7, s41, 0
	v_add_u32_e32 v4, v15, v4
	s_add_u32 s8, s40, 0x6880000
	v_and_b32_e32 v5, 3, v15
	v_lshrrev_b32_e32 v6, 2, v4
	v_lshlrev_b32_e32 v7, 1, v4
	v_and_b32_e32 v2, 0xc0, v2
	s_addc_u32 s9, s41, 0
	s_ashr_i32 s5, s46, 6
	v_and_or_b32 v5, v4, s18, v5
	v_and_b32_e32 v6, 4, v6
	v_and_b32_e32 v7, 24, v7
	v_sub_u32_e32 v1, v1, v2
	s_ashr_i32 s4, s46, 8
	s_lshl_b32 s17, s5, 10
	v_or3_b32 v5, v5, v6, v7
	v_lshlrev_b32_e32 v6, 5, v16
	v_ashrrev_i16_sdwa v1, v244, sext(v1) dst_sel:DWORD dst_unused:UNUSED_PAD src0_sel:DWORD src1_sel:BYTE_0
	v_readlane_b32 s18, v254, 53
	v_and_b32_e32 v6, 32, v6
	v_bfe_i32 v17, v1, 0, 16
	v_readlane_b32 s19, v254, 54
	s_add_u32 s58, s8, s18
	v_add_lshl_u32 v1, v6, v17, 1
	s_addc_u32 s59, s9, s19
	s_add_i32 s18, s17, 0
	v_lshl_add_u32 v2, v5, 10, v1
	s_add_i32 m0, s18, 0x10000
	v_lshl_add_u32 v168, v4, 10, v1
	global_load_lds_dwordx4 v2, s[58:59]
	s_add_i32 m0, s18, 0x12000
	s_add_u32 s20, s58, 0x20000
	global_load_lds_dwordx4 v164, s[58:59]
	s_addc_u32 s21, s59, 0
	s_add_i32 m0, s18, 0x14000
	v_mov_b32_e32 v165, v3
	global_load_lds_dwordx4 v2, s[20:21]
	s_add_i32 m0, s18, 0x16000
	v_mov_b32_e32 v169, v3
	global_load_lds_dwordx4 v164, s[20:21]
	v_readlane_b32 s20, v252, 14
	v_readlane_b32 s21, v252, 15
	s_add_u32 s56, s6, s20
	s_addc_u32 s57, s7, s21
	s_add_i32 s19, s18, 0x2000
	s_mov_b32 m0, s18
	s_add_u32 s22, s56, 0x20000
	global_load_lds_dwordx4 v168, s[56:57]
	s_mov_b32 m0, s19
	s_addc_u32 s23, s57, 0
	s_add_i32 s20, s18, 0x4000
	global_load_lds_dwordx4 v166, s[56:57]
	s_mov_b32 m0, s20
	s_add_i32 s21, s18, 0x6000
	global_load_lds_dwordx4 v168, s[22:23]
	s_mov_b32 m0, s21
	v_mov_b32_e32 v167, v3
	global_load_lds_dwordx4 v166, s[22:23]
	s_cmp_eq_u32 s4, 1
	v_lshl_add_u64 v[10:11], s[58:59], 0, v[2:3]
	v_lshl_add_u64 v[8:9], s[58:59], 0, v[164:165]
	v_lshl_add_u64 v[4:5], s[56:57], 0, v[168:169]
	s_cselect_b64 s[38:39], -1, 0
	s_cmp_lg_u32 s4, 1
	v_lshl_add_u64 v[6:7], s[56:57], 0, v[166:167]
	s_cbranch_scc1 .LBB0_1683
	s_barrier

; #define PG8_STAGE(bufoff, gbase, voff) do { _Pragma("unroll") for (int _i = 0; _i < 2; ++_i) \
;         __builtin_amdgcn_global_load_lds((const unsigned*)((const char*)(gbase) + (voff)[_i]), (PG8_LAS unsigned*)(lds + (bufoff) + ldsw + _i * 8192), 16, 0, 0); } while (0)
; #define PG8_BAR __builtin_amdgcn_s_barrier()
; template <class Epi, class Sched, bool ALIGN_EPI = false, bool SP2 = false, bool FP8 = false, bool ABLK = false>
; __device__ __forceinline__ void gemm_phase(PG8_LAS unsigned char* lds, const Gemm g, const Sched& S, const Epi& E) {
;     int tid_ = threadIdx.x; asm volatile("" : "+v"(tid_));
;     const int tid = tid_, wid = __builtin_amdgcn_readfirstlane(tid >> 6), lane = tid & 63, wr = wid >> 2, wc = wid & 3, fr = lane & 15, fq = lane >> 4;
;     const int K = g.K, nt = K / BK;
;     unsigned voffA[2], voffB[2];
; #pragma unroll
;     for (int i = 0; i < 2; ++i) { int R, C; stage_rc(tid * 16 + i * 8192, R, C); const int Rb = Epi::PERM ? ((R & ~31) + perm32(R & 31)) : R;
;         voffA[i] = ABLK ? (unsigned)(((((R >> 6) * 4 + (C >> 4)) * 8 + ((R >> 4) & 3)) * 64 + ((C >> 3) & 1) * 32 + (R & 15) * 2) * 8) : (unsigned)(R * K + C) * 2u; voffB[i] = (unsigned)(Rb * K + C) * 2u; }
;     const size_t kstep = (size_t)(BK * 2);
;     const size_t hstep = (size_t)HALF * K * 2;
;     const size_t kstepA = ABLK ? (size_t)32768 : kstep, hstepA = ABLK ? (size_t)2048 : hstep;
;     const size_t tstep = 2 * hstep;
;     const unsigned ldsw = (unsigned)wid * 1024u;
;     const int aoff = lds_byte(wr * 64 + fr, fq * 8), boff = lds_byte(wc * 32 + fr, fq * 8);
;     ...
;     Unit cur, nxt; int ui = 0;
;     if (!S.next(0, cur)) return;
;     f32x4 acc[2][2][4][2];
; #pragma unroll
;     for (int a = 0; a < 2; ++a)
; #pragma unroll
;         for (int b = 0; b < 2; ++b)
; #pragma unroll
;             for (int m = 0; m < 4; ++m)
; #pragma unroll
;                 for (int n = 0; n < 2; ++n) acc[a][b][m][n] = (f32x4){0.f, 0.f, 0.f, 0.f};
;     bf16x8 At[4][2], B0[2][2], B1[2][2];
;     const char* cA = (const char*)g.A + (size_t)cur.pm * tstep; const char* cB = (const char*)g.Bt + (size_t)cur.pn * tstep;
;     S.a_ready(cur);
;     if constexpr (SP2) {
;         PG8_STAGE(PG8_SB(0, 0), cB, voffB); PG8_STAGE(PG8_SB(0, 1), cB + hstep, voffB); PG8_STAGE(PG8_SA(0, 0), cA, voffA); PG8_STAGE(PG8_SA(0, 1), cA + hstepA, voffA);
;         if (wr == 1) PG8_BAR;
.LBB0_1814:
	v_readlane_b32 s6, v252, 25
	v_mov_b32_e32 v1, v0
	s_mov_b64 s[4:5], s[66:67]
	s_and_b32 s11, s2, 8
	s_cmp_eq_u32 s11, 0
	s_cbranch_scc1 .Lstag_8
	s_sleep 64
.Lstag_8:
	v_mov_b32_e32 v13, v0
	v_readlane_b32 s7, v252, 26
	s_and_b64 vcc, exec, s[6:7]
	v_readfirstlane_b32 s40, v13
	s_cbranch_vccnz .LBB0_1854
	v_lshlrev_b32_e32 v1, 4, v13
	v_add_u32_e32 v2, 0x2000, v1
	v_ashrrev_i32_e32 v4, 31, v2
	v_lshrrev_b32_e32 v4, 22, v4
	v_add_u32_e32 v4, v2, v4
	v_ashrrev_i32_e32 v4, 10, v4
	s_waitcnt lgkmcnt(0)
	v_mul_i32_i24_e32 v5, 0x400, v4
	v_sub_u32_e32 v2, v2, v5
	v_lshrrev_b32_e32 v5, 4, v2
	v_bitop3_b32 v2, v5, v2, 32 bitop3:0x6c
	v_ashrrev_i32_e32 v5, 31, v2
	v_lshrrev_b32_e32 v5, 26, v5
	v_add_u32_e32 v5, v2, v5
	v_lshlrev_b32_e32 v7, 3, v4
	v_ashrrev_i32_e32 v6, 6, v5
	v_and_b32_e32 v7, -16, v7
	v_add_u32_e32 v8, v6, v7
	v_and_b32_e32 v6, 3, v6
	s_mov_b32 s18, 0x1ffffe0
	v_lshrrev_b32_e32 v7, 2, v8
	v_lshlrev_b32_e32 v9, 1, v8
	v_and_b32_e32 v5, 0xc0, v5
	v_and_or_b32 v6, v8, s18, v6
	v_and_b32_e32 v7, 4, v7
	v_and_b32_e32 v9, 24, v9
	v_lshlrev_b32_e32 v4, 5, v4
	v_sub_u32_e32 v2, v2, v5
	v_or3_b32 v6, v6, v7, v9
	s_movk_i32 s19, 0x580
	v_and_b32_e32 v4, 32, v4
	v_ashrrev_i16_sdwa v2, v244, sext(v2) dst_sel:DWORD dst_unused:UNUSED_PAD src0_sel:DWORD src1_sel:BYTE_0
	v_mul_lo_u32 v6, v6, s19
	v_add_u32_sdwa v2, v4, sext(v2) dst_sel:DWORD dst_unused:UNUSED_PAD src0_sel:DWORD src1_sel:WORD_0
	s_waitcnt vmcnt(0)
	v_add_lshl_u32 v164, v6, v2, 1
	v_lshrrev_b32_e32 v9, 4, v2
	v_lshlrev_b32_e32 v2, 5, v2
	v_and_b32_e32 v11, 0x100, v2
	v_lshlrev_b32_e32 v2, 4, v8
	v_and_b32_e32 v12, 0xf0, v2
	v_bfe_i32 v2, v13, 27, 1
	v_lshrrev_b32_e32 v2, 22, v2
	s_load_dwordx2 s[38:39], s[4:5], 0xd0
	v_add_u32_e32 v2, v1, v2
	v_and_b32_e32 v2, 0xfffffc00, v2
	v_lshlrev_b32_e32 v5, 5, v8
	v_sub_u32_e32 v1, v1, v2
	v_readlane_b32 s4, v252, 18
	v_and_b32_e32 v10, 0x600, v5
	v_lshrrev_b32_e32 v2, 4, v1
	v_ashrrev_i32_e32 v5, 31, v13
	s_mul_i32 s4, s4, 0x2d80000
	v_lshrrev_b32_e32 v4, 4, v8
	v_bitop3_b32 v1, v2, v1, 32 bitop3:0x6c
	v_lshrrev_b32_e32 v5, 26, v5
	v_readlane_b32 s5, v252, 19
	s_waitcnt lgkmcnt(0)
	s_add_u32 s4, s38, s4
	v_and_b32_e32 v4, 0xffffc, v4
	v_ashrrev_i32_e32 v2, 31, v1
	v_add_u32_e32 v5, v13, v5
	s_addc_u32 s5, s39, 0
	v_add_u32_e32 v4, v9, v4
	v_lshrrev_b32_e32 v2, 26, v2
	v_ashrrev_i32_e32 v5, 6, v5
	s_add_u32 s6, s38, 0xba00000
	v_lshl_or_b32 v4, v4, 12, v10
	v_add_u32_e32 v2, v1, v2
	v_lshlrev_b32_e32 v6, 3, v5
	s_addc_u32 s7, s39, 0
	v_or3_b32 v166, v4, v11, v12
	v_ashrrev_i32_e32 v4, 6, v2
	v_and_b32_e32 v6, -16, v6
	s_add_u32 s8, s4, 0x4600000
	v_add_u32_e32 v14, v4, v6
	s_addc_u32 s9, s5, 0
	s_ashr_i32 s5, s40, 6
	v_and_b32_e32 v4, 3, v4
	v_lshrrev_b32_e32 v6, 2, v14
	v_lshlrev_b32_e32 v7, 1, v14
	v_and_b32_e32 v2, 0xc0, v2
	s_ashr_i32 s4, s40, 8
	s_lshl_b32 s17, s5, 10
	v_and_or_b32 v4, v14, s18, v4
	v_and_b32_e32 v6, 4, v6
	v_and_b32_e32 v7, 24, v7
	v_lshlrev_b32_e32 v5, 5, v5
	v_sub_u32_e32 v1, v1, v2
	v_readlane_b32 s18, v254, 59
	v_or3_b32 v4, v4, v6, v7
	v_and_b32_e32 v5, 32, v5
	v_ashrrev_i16_sdwa v1, v244, sext(v1) dst_sel:DWORD dst_unused:UNUSED_PAD src0_sel:DWORD src1_sel:BYTE_0
	s_add_u32 s54, s8, s18
	v_readlane_b32 s18, v254, 57
	v_mul_lo_u32 v4, v4, s19
	v_add_u32_sdwa v1, v5, sext(v1) dst_sel:DWORD dst_unused:UNUSED_PAD src0_sel:DWORD src1_sel:WORD_0
	s_addc_u32 s55, s9, s18
	s_add_i32 s18, s17, 0
	v_add_lshl_u32 v2, v4, v1, 1
	s_add_i32 m0, s18, 0x10000
	v_lshrrev_b32_e32 v4, 4, v14
	global_load_lds_dwordx4 v2, s[54:55]
	s_add_i32 m0, s18, 0x12000
	s_add_u32 s20, s54, 0x58000
	v_lshrrev_b32_e32 v15, 4, v1
	v_and_b32_e32 v4, 0xffffc, v4
	v_lshlrev_b32_e32 v5, 5, v14
	v_lshlrev_b32_e32 v1, 5, v1
	global_load_lds_dwordx4 v164, s[54:55]
	s_addc_u32 s21, s55, 0
	s_add_i32 m0, s18, 0x14000
	v_add_u32_e32 v4, v15, v4
	v_and_b32_e32 v16, 0x600, v5
	v_and_b32_e32 v17, 0x100, v1
	v_lshlrev_b32_e32 v1, 4, v14
	global_load_lds_dwordx4 v2, s[20:21]
	s_add_i32 m0, s18, 0x16000
	v_readlane_b32 s19, v254, 56
	v_lshl_or_b32 v4, v4, 12, v16
	v_and_b32_e32 v18, 0xf0, v1
	s_add_u32 s52, s6, s19
	v_readlane_b32 s19, v254, 55
	v_or3_b32 v168, v4, v17, v18
	global_load_lds_dwordx4 v164, s[20:21]
	s_addc_u32 s53, s7, s19
	v_mov_b32_e32 v169, v3
	s_mov_b32 m0, s18
	s_add_i32 s19, s18, 0x2000
	v_lshl_add_u64 v[4:5], s[52:53], 0, v[168:169]
	global_load_lds_dwordx4 v168, s[52:53]
	v_mov_b32_e32 v167, v3
	s_mov_b32 m0, s19
	s_add_i32 s20, s18, 0x4000
	v_lshl_add_u64 v[6:7], s[52:53], 0, v[166:167]
	global_load_lds_dwordx4 v166, s[52:53]
	v_lshl_add_u64 v[4:5], v[4:5], 0, s[24:25]
	s_mov_b32 m0, s20
	s_add_i32 s21, s18, 0x6000
	global_load_lds_dwordx4 v[4:5], off
	v_lshl_add_u64 v[4:5], v[6:7], 0, s[24:25]
	s_mov_b32 m0, s21
	v_mov_b32_e32 v165, v3
	global_load_lds_dwordx4 v[4:5], off
	s_cmp_eq_u32 s4, 1
	v_lshl_add_u64 v[4:5], s[54:55], 0, v[2:3]
	s_cselect_b64 s[42:43], -1, 0
	s_cmp_lg_u32 s4, 1
	v_lshl_add_u64 v[6:7], s[54:55], 0, v[164:165]
	s_cbranch_scc1 .LBB0_1817
	s_barrier
